# plus: MoE weight-load order alternates by row-tile parity among the workgroups sharing an expert weight tile
# baseline (speedup 1.0000x reference)
.LBB0_717:
	s_cmp_lt_i32 s76, s43
	s_cselect_b32 s45, s76, s44
	s_cmp_lt_i32 s45, 0
	s_cbranch_scc1 .LBB0_741
	s_add_u32 s8, s10, 0x1cd90000
	s_addc_u32 s9, s11, 0
	s_add_u32 s46, s10, 0x3adc0000
	s_addc_u32 s47, s11, 0
	s_abs_i32 s48, s42
	v_cvt_f32_u32_e32 v1, s48
	s_sub_i32 s2, 0, s48
	s_abs_i32 s1, s45
	s_ashr_i32 s0, s45, 31
	v_rcp_iflag_f32_e32 v1, v1
	s_ashr_i32 s49, s42, 31
	s_lshr_b32 s5, s4, 6
	s_xor_b32 s0, s0, s49
	v_mul_f32_e32 v1, 0x4f7ffffe, v1
	v_cvt_u32_f32_e32 v1, v1
	v_bfe_u32 v3, v0, 2, 4
	v_lshrrev_b32_e32 v4, 3, v0
	s_movk_i32 s61, 0x81
	v_readfirstlane_b32 s50, v1
	s_mul_i32 s2, s2, s50
	s_mul_hi_u32 s2, s50, s2
	s_add_i32 s50, s50, s2
	s_lshr_b32 s89, s45, 3
	s_lshl_b32 s89, s89, 2
	s_add_i32 s89, s89, 0x202e0
	v_mov_b32_e32 v222, s89
	ds_read_b32 v222, v222
	s_waitcnt lgkmcnt(0)
	v_lshlrev_b32_e32 v222, 2, v222
	v_add_u32_e32 v222, 0x20240, v222
	ds_read2_b32 v[252:253], v222 offset1:1
	s_waitcnt lgkmcnt(0)
	v_readfirstlane_b32 s90, v252
	v_readfirstlane_b32 s91, v253
	s_nop 3
	s_sub_i32 s91, s91, s90
	s_lshl_b32 s92, s90, 3
	s_sub_i32 s92, s45, s92
	s_mov_b32 s18, 0
	s_cmp_ge_u32 s92, s91
	s_cselect_b32 s93, s91, 0
	s_cselect_b32 s94, 1, 0
	s_sub_i32 s92, s92, s93
	s_add_i32 s18, s18, s94
	s_cmp_ge_u32 s92, s91
	s_cselect_b32 s93, s91, 0
	s_cselect_b32 s94, 1, 0
	s_sub_i32 s92, s92, s93
	s_add_i32 s18, s18, s94
	s_cmp_ge_u32 s92, s91
	s_cselect_b32 s93, s91, 0
	s_cselect_b32 s94, 1, 0
	s_sub_i32 s92, s92, s93
	s_add_i32 s18, s18, s94
	s_cmp_ge_u32 s92, s91
	s_cselect_b32 s93, s91, 0
	s_cselect_b32 s94, 1, 0
	s_sub_i32 s92, s92, s93
	s_add_i32 s18, s18, s94
	s_cmp_ge_u32 s92, s91
	s_cselect_b32 s93, s91, 0
	s_cselect_b32 s94, 1, 0
	s_sub_i32 s92, s92, s93
	s_add_i32 s18, s18, s94
	s_cmp_ge_u32 s92, s91
	s_cselect_b32 s93, s91, 0
	s_cselect_b32 s94, 1, 0
	s_sub_i32 s92, s92, s93
	s_add_i32 s18, s18, s94
	s_cmp_ge_u32 s92, s91
	s_cselect_b32 s93, s91, 0
	s_cselect_b32 s94, 1, 0
	s_sub_i32 s92, s92, s93
	s_add_i32 s18, s18, s94
	s_add_i32 s12, s90, s92
	s_and_b32 s99, s12, 1
	s_lshl_b32 s0, s12, 2
	s_add_i32 s0, s0, 0
	s_add_i32 s0, s0, 0x202e0
	v_mov_b32_e32 v1, s0
	ds_read_b32 v5, v1
	v_and_or_b32 v1, v4, 48, v3
	v_or_b32_e32 v4, 64, v4
	s_movk_i32 s0, 0x70
	v_and_or_b32 v186, v4, s0, v3
	s_waitcnt lgkmcnt(0)
	v_lshlrev_b32_e32 v3, 2, v5
	v_add_u32_e32 v3, 0, v3
	v_add_u32_e32 v4, 0x20240, v3
	ds_read_b32 v4, v4
	v_add_u32_e32 v3, 0x201c0, v3
	ds_read_b32 v3, v3
	v_readfirstlane_b32 s2, v5
	s_ashr_i32 s3, s2, 31
	s_waitcnt lgkmcnt(1)
	v_sub_u32_e32 v4, s12, v4
	v_lshlrev_b32_e32 v18, 8, v4
	v_lshlrev_b32_e32 v4, 6, v5
	s_waitcnt lgkmcnt(0)
	v_add_u32_e32 v19, -1, v3
	v_add_u32_e32 v4, 0, v4
	v_or_b32_e32 v22, v18, v1
	v_add_u32_e32 v20, 0x208e0, v4
	v_min_i32_e32 v22, v22, v19
	ds_read2_b32 v[4:5], v20 offset0:1 offset1:2
	ds_read2_b32 v[6:7], v20 offset0:3 offset1:4
	ds_read2_b32 v[8:9], v20 offset0:5 offset1:6
	ds_read2_b32 v[10:11], v20 offset0:7 offset1:8
	ds_read2_b32 v[12:13], v20 offset0:9 offset1:10
	ds_read2_b32 v[14:15], v20 offset0:11 offset1:12
	ds_read2_b32 v[16:17], v20 offset0:13 offset1:14
	ds_read_b32 v21, v20 offset:60
	s_waitcnt lgkmcnt(7)
	v_cmp_ge_i32_e32 vcc, v22, v4
	v_or_b32_e32 v25, v18, v186
	v_min_i32_e32 v25, v25, v19
	v_cndmask_b32_e64 v23, 0, 1, vcc
	v_cmp_ge_i32_e32 vcc, v22, v5
	v_or_b32_e32 v28, 0x80, v18
	v_or_b32_e32 v29, v28, v1
	v_cndmask_b32_e64 v24, 0, 1, vcc
	s_waitcnt lgkmcnt(6)
	v_cmp_ge_i32_e32 vcc, v22, v6
	v_min_i32_e32 v29, v29, v19
	v_or_b32_e32 v28, v28, v186
	v_addc_co_u32_e32 v23, vcc, v23, v24, vcc
	v_cmp_ge_i32_e32 vcc, v22, v7
	v_min_i32_e32 v19, v28, v19
	s_lshl_b64 s[0:1], s[2:3], 15
	v_cndmask_b32_e64 v24, 0, 1, vcc
	s_waitcnt lgkmcnt(5)
	v_cmp_ge_i32_e32 vcc, v22, v8
	s_add_u32 s0, s46, s0
	s_addc_u32 s1, s47, s1
	v_addc_co_u32_e32 v23, vcc, v23, v24, vcc
	v_cmp_ge_i32_e32 vcc, v22, v9
	v_sub_u32_e32 v3, v3, v18
	s_nop 0
	v_cndmask_b32_e64 v24, 0, 1, vcc
	s_waitcnt lgkmcnt(4)
	v_cmp_ge_i32_e32 vcc, v22, v10
	s_nop 1
	v_addc_co_u32_e32 v23, vcc, v23, v24, vcc
	v_cmp_ge_i32_e32 vcc, v22, v11
	s_nop 1
	v_cndmask_b32_e64 v24, 0, 1, vcc
	s_waitcnt lgkmcnt(3)
	v_cmp_ge_i32_e32 vcc, v22, v12
	s_nop 1
	v_addc_co_u32_e32 v23, vcc, v23, v24, vcc
	v_cmp_ge_i32_e32 vcc, v22, v13
	s_nop 1
	v_cndmask_b32_e64 v24, 0, 1, vcc
	s_waitcnt lgkmcnt(2)
	v_cmp_ge_i32_e32 vcc, v22, v14
	s_nop 1
	v_addc_co_u32_e32 v23, vcc, v23, v24, vcc
	v_cmp_ge_i32_e32 vcc, v22, v15
	s_nop 1
	v_cndmask_b32_e64 v24, 0, 1, vcc
	s_waitcnt lgkmcnt(1)
	v_cmp_ge_i32_e32 vcc, v22, v16
	s_nop 1
	v_addc_co_u32_e32 v23, vcc, v23, v24, vcc
	v_cmp_ge_i32_e32 vcc, v22, v17
	s_nop 1
	v_cndmask_b32_e64 v24, 0, 1, vcc
	s_waitcnt lgkmcnt(0)
	v_cmp_ge_i32_e32 vcc, v22, v21
	s_nop 1
	v_addc_co_u32_e32 v23, vcc, v23, v24, vcc
	v_cmp_ge_i32_e32 vcc, v25, v4
	v_lshl_add_u32 v24, v23, 2, v20
	ds_read_b32 v24, v24
	v_cndmask_b32_e64 v26, 0, 1, vcc
	v_cmp_ge_i32_e32 vcc, v25, v5
	s_nop 1
	v_cndmask_b32_e64 v27, 0, 1, vcc
	v_cmp_ge_i32_e32 vcc, v25, v6
	s_nop 1
	v_addc_co_u32_e32 v26, vcc, v26, v27, vcc
	v_cmp_ge_i32_e32 vcc, v25, v7
	s_nop 1
	v_cndmask_b32_e64 v27, 0, 1, vcc
	v_cmp_ge_i32_e32 vcc, v25, v8
	s_nop 1
	v_addc_co_u32_e32 v26, vcc, v26, v27, vcc
	v_cmp_ge_i32_e32 vcc, v25, v9
	s_nop 1
	v_cndmask_b32_e64 v27, 0, 1, vcc
	v_cmp_ge_i32_e32 vcc, v25, v10
	s_nop 1
	v_addc_co_u32_e32 v26, vcc, v26, v27, vcc
	v_cmp_ge_i32_e32 vcc, v25, v11
	s_nop 1
	v_cndmask_b32_e64 v27, 0, 1, vcc
	v_cmp_ge_i32_e32 vcc, v25, v12
	s_nop 1
	v_addc_co_u32_e32 v26, vcc, v26, v27, vcc
	v_cmp_ge_i32_e32 vcc, v25, v13
	s_nop 1
	v_cndmask_b32_e64 v27, 0, 1, vcc
	v_cmp_ge_i32_e32 vcc, v25, v14
	s_nop 1
	v_addc_co_u32_e32 v26, vcc, v26, v27, vcc
	v_cmp_ge_i32_e32 vcc, v25, v15
	s_nop 1
	v_cndmask_b32_e64 v27, 0, 1, vcc
	v_cmp_ge_i32_e32 vcc, v25, v16
	s_nop 1
	v_addc_co_u32_e32 v26, vcc, v26, v27, vcc
	v_cmp_ge_i32_e32 vcc, v25, v17
	s_nop 1
	v_cndmask_b32_e64 v27, 0, 1, vcc
	v_cmp_ge_i32_e32 vcc, v25, v21
	s_nop 1
	v_addc_co_u32_e32 v26, vcc, v26, v27, vcc
	v_cmp_ge_i32_e32 vcc, v29, v4
	v_lshl_add_u32 v27, v26, 2, v20
	s_nop 0
	v_cndmask_b32_e64 v30, 0, 1, vcc
	v_cmp_ge_i32_e32 vcc, v29, v5
	s_nop 1
	v_cndmask_b32_e64 v31, 0, 1, vcc
	v_cmp_ge_i32_e32 vcc, v29, v6
	s_nop 1
	v_addc_co_u32_e32 v30, vcc, v30, v31, vcc
	v_cmp_ge_i32_e32 vcc, v29, v7
	s_nop 1
	v_cndmask_b32_e64 v31, 0, 1, vcc
	v_cmp_ge_i32_e32 vcc, v29, v8
	s_nop 1
	v_addc_co_u32_e32 v30, vcc, v30, v31, vcc
	v_cmp_ge_i32_e32 vcc, v29, v9
	s_nop 1
	v_cndmask_b32_e64 v31, 0, 1, vcc
	v_cmp_ge_i32_e32 vcc, v29, v10
	s_nop 1
	v_addc_co_u32_e32 v30, vcc, v30, v31, vcc
	v_cmp_ge_i32_e32 vcc, v29, v11
	s_nop 1
	v_cndmask_b32_e64 v31, 0, 1, vcc
	v_cmp_ge_i32_e32 vcc, v29, v12
	s_nop 1
	v_addc_co_u32_e32 v30, vcc, v30, v31, vcc
	v_cmp_ge_i32_e32 vcc, v29, v13
	s_nop 1
	v_cndmask_b32_e64 v31, 0, 1, vcc
	v_cmp_ge_i32_e32 vcc, v29, v14
	s_nop 1
	v_addc_co_u32_e32 v30, vcc, v30, v31, vcc
	v_cmp_ge_i32_e32 vcc, v29, v15
	s_nop 1
	v_cndmask_b32_e64 v31, 0, 1, vcc
	v_cmp_ge_i32_e32 vcc, v29, v16
	s_nop 1
	v_addc_co_u32_e32 v30, vcc, v30, v31, vcc
	v_cmp_ge_i32_e32 vcc, v29, v17
	s_nop 1
	v_cndmask_b32_e64 v31, 0, 1, vcc
	v_cmp_ge_i32_e32 vcc, v29, v21
	s_nop 1
	v_addc_co_u32_e32 v30, vcc, v30, v31, vcc
	v_cmp_ge_i32_e32 vcc, v19, v4
	v_lshl_add_u32 v31, v30, 2, v20
	s_nop 0
	v_cndmask_b32_e64 v4, 0, 1, vcc
	v_cmp_ge_i32_e32 vcc, v19, v5
	s_nop 1
	v_cndmask_b32_e64 v5, 0, 1, vcc
	v_cmp_ge_i32_e32 vcc, v19, v6
	s_nop 1
	v_addc_co_u32_e32 v4, vcc, v4, v5, vcc
	v_cmp_ge_i32_e32 vcc, v19, v7
	s_nop 1
	v_cndmask_b32_e64 v5, 0, 1, vcc
	v_cmp_ge_i32_e32 vcc, v19, v8
	s_nop 1
	v_addc_co_u32_e32 v4, vcc, v4, v5, vcc
	v_cmp_ge_i32_e32 vcc, v19, v9
	s_nop 1
	v_cndmask_b32_e64 v5, 0, 1, vcc
	v_cmp_ge_i32_e32 vcc, v19, v10
	s_nop 1
	v_addc_co_u32_e32 v4, vcc, v4, v5, vcc
	v_cmp_ge_i32_e32 vcc, v19, v11
	s_nop 1
	v_cndmask_b32_e64 v5, 0, 1, vcc
	v_cmp_ge_i32_e32 vcc, v19, v12
	s_nop 1
	v_addc_co_u32_e32 v4, vcc, v4, v5, vcc
	v_cmp_ge_i32_e32 vcc, v19, v13
	s_nop 1
	v_cndmask_b32_e64 v5, 0, 1, vcc
	v_cmp_ge_i32_e32 vcc, v19, v14
	s_nop 1
	v_addc_co_u32_e32 v4, vcc, v4, v5, vcc
	v_cmp_ge_i32_e32 vcc, v19, v15
	s_nop 1
	v_cndmask_b32_e64 v5, 0, 1, vcc
	v_cmp_ge_i32_e32 vcc, v19, v16
	s_nop 1
	v_addc_co_u32_e32 v4, vcc, v4, v5, vcc
	v_cmp_ge_i32_e32 vcc, v19, v17
	s_nop 1
	v_cndmask_b32_e64 v5, 0, 1, vcc
	v_cmp_ge_i32_e32 vcc, v19, v21
	s_nop 1
	v_addc_co_u32_e32 v8, vcc, v4, v5, vcc
	v_lshl_add_u32 v4, v8, 2, v20
	ds_read_b32 v6, v27
	ds_read_b32 v9, v31
	ds_read_b32 v10, v4
	s_waitcnt lgkmcnt(3)
	v_sub_u32_e32 v4, v22, v24
	v_lshl_add_u32 v4, v23, 9, v4
	s_waitcnt lgkmcnt(2)
	v_sub_u32_e32 v6, v25, v6
	v_ashrrev_i32_e32 v5, 31, v4
	v_lshl_add_u32 v6, v26, 9, v6
	v_lshl_add_u64 v[4:5], v[4:5], 2, s[0:1]
	v_ashrrev_i32_e32 v7, 31, v6
	v_lshl_add_u64 v[6:7], v[6:7], 2, s[0:1]
	global_load_dword v11, v[4:5], off
	global_load_dword v12, v[6:7], off
	v_lshlrev_b32_e32 v4, 4, v0
	v_and_b32_e32 v5, 32, v0
	v_bitop3_b32 v4, v4, v5, 48 bitop3:0x6c
	v_and_or_b32 v187, v0, 64, v4
	s_waitcnt lgkmcnt(1)
	v_sub_u32_e32 v4, v29, v9
	v_lshl_add_u32 v6, v8, 9, v19
	v_lshl_add_u32 v4, v30, 9, v4
	s_waitcnt lgkmcnt(0)
	v_sub_u32_e32 v6, v6, v10
	v_ashrrev_i32_e32 v5, 31, v4
	v_ashrrev_i32_e32 v7, 31, v6
	v_lshl_add_u64 v[4:5], v[4:5], 2, s[0:1]
	v_lshl_add_u64 v[6:7], v[6:7], 2, s[0:1]
	s_lshl_b32 s0, s5, 10
	global_load_dword v8, v[4:5], off
	global_load_dword v9, v[6:7], off
	s_waitcnt vmcnt(0)
	s_add_i32 s51, s0, 0
	s_waitcnt lgkmcnt(0)
	s_barrier
	s_mov_b32 m0, s51
	s_add_i32 s60, s51, 0x2000
	v_cmp_gt_i32_e64 s[0:1], s61, v3
	s_and_b64 vcc, exec, s[0:1]
	s_waitcnt vmcnt(3)
	v_lshl_or_b32 v178, v11, 12, v187
	s_waitcnt vmcnt(2)
	v_lshl_or_b32 v180, v12, 12, v187
	global_load_lds_dwordx4 v178, s[8:9]
	s_mov_b32 m0, s60
	s_waitcnt vmcnt(0)
	v_lshl_or_b32 v182, v8, 12, v187
	global_load_lds_dwordx4 v180, s[8:9]
	v_lshl_or_b32 v184, v9, 12, v187
	s_cbranch_vccnz .LBB0_720
	s_add_i32 m0, s51, 0x4000
	s_nop 0
	global_load_lds_dwordx4 v182, s[8:9]
	s_add_i32 m0, s51, 0x6000
	s_nop 0
	global_load_lds_dwordx4 v184, s[8:9]

.LBB0_721:
	s_add_i32 s0, s45, s33
	s_cmp_lt_i32 s45, s43
	s_cselect_b32 s1, s44, -1
	s_cmp_lt_i32 s0, s43
	s_cselect_b32 s45, s0, s1
	s_cmp_lt_i32 s45, 0
	s_cselect_b64 s[14:15], -1, 0
	s_and_b64 vcc, exec, s[14:15]
	v_mov_b32_e32 v209, v178
	v_mov_b32_e32 v210, v180
	v_mov_b32_e32 v211, v182
	v_mov_b32_e32 v212, v184
	s_mov_b32 s16, s18
	s_cbranch_vccnz .LBB0_723
	s_lshr_b32 s89, s45, 3
	s_lshl_b32 s89, s89, 2
	s_add_i32 s89, s89, 0x202e0
	v_mov_b32_e32 v222, s89
	ds_read_b32 v222, v222
	s_waitcnt lgkmcnt(0)
	v_lshlrev_b32_e32 v222, 2, v222
	v_add_u32_e32 v222, 0x20240, v222
	ds_read2_b32 v[252:253], v222 offset1:1
	s_waitcnt lgkmcnt(0)
	v_readfirstlane_b32 s90, v252
	v_readfirstlane_b32 s91, v253
	s_nop 3
	s_sub_i32 s91, s91, s90
	s_lshl_b32 s92, s90, 3
	s_sub_i32 s92, s45, s92
	s_mov_b32 s16, 0
	s_cmp_ge_u32 s92, s91
	s_cselect_b32 s93, s91, 0
	s_cselect_b32 s94, 1, 0
	s_sub_i32 s92, s92, s93
	s_add_i32 s16, s16, s94
	s_cmp_ge_u32 s92, s91
	s_cselect_b32 s93, s91, 0
	s_cselect_b32 s94, 1, 0
	s_sub_i32 s92, s92, s93
	s_add_i32 s16, s16, s94
	s_cmp_ge_u32 s92, s91
	s_cselect_b32 s93, s91, 0
	s_cselect_b32 s94, 1, 0
	s_sub_i32 s92, s92, s93
	s_add_i32 s16, s16, s94
	s_cmp_ge_u32 s92, s91
	s_cselect_b32 s93, s91, 0
	s_cselect_b32 s94, 1, 0
	s_sub_i32 s92, s92, s93
	s_add_i32 s16, s16, s94
	s_cmp_ge_u32 s92, s91
	s_cselect_b32 s93, s91, 0
	s_cselect_b32 s94, 1, 0
	s_sub_i32 s92, s92, s93
	s_add_i32 s16, s16, s94
	s_cmp_ge_u32 s92, s91
	s_cselect_b32 s93, s91, 0
	s_cselect_b32 s94, 1, 0
	s_sub_i32 s92, s92, s93
	s_add_i32 s16, s16, s94
	s_cmp_ge_u32 s92, s91
	s_cselect_b32 s93, s91, 0
	s_cselect_b32 s94, 1, 0
	s_sub_i32 s92, s92, s93
	s_add_i32 s16, s16, s94
	s_add_i32 s4, s90, s92
	s_and_b32 s100, s4, 1
	s_lshl_b32 s0, s4, 2
	s_add_i32 s0, s0, 0
	s_add_i32 s0, s0, 0x202e0
	v_mov_b32_e32 v30, s0
	ds_read_b32 v30, v30
	s_ashr_i32 s17, s16, 31
	s_waitcnt lgkmcnt(0)
	v_lshlrev_b32_e32 v31, 2, v30
	v_add_u32_e32 v31, 0, v31
	v_add_u32_e32 v32, 0x20240, v31
	ds_read_b32 v32, v32
	v_add_u32_e32 v31, 0x201c0, v31
	ds_read_b32 v48, v31
	v_readfirstlane_b32 s2, v30
	v_lshlrev_b32_e32 v30, 6, v30
	s_waitcnt lgkmcnt(0)
	v_sub_u32_e32 v31, s4, v32
	v_lshlrev_b32_e32 v49, 8, v31
	v_add_u32_e32 v50, -1, v48
	v_add_u32_e32 v30, 0, v30
	v_or_b32_e32 v53, v49, v1
	v_add_u32_e32 v51, 0x208e0, v30
	v_min_i32_e32 v53, v53, v50
	ds_read2_b32 v[30:31], v51 offset0:1 offset1:2
	ds_read2_b32 v[32:33], v51 offset0:3 offset1:4
	ds_read2_b32 v[38:39], v51 offset0:5 offset1:6
	ds_read2_b32 v[40:41], v51 offset0:7 offset1:8
	ds_read2_b32 v[42:43], v51 offset0:9 offset1:10
	ds_read2_b32 v[44:45], v51 offset0:11 offset1:12
	ds_read2_b32 v[46:47], v51 offset0:13 offset1:14
	ds_read_b32 v52, v51 offset:60
	s_waitcnt lgkmcnt(0)
	v_cmp_ge_i32_e32 vcc, v53, v30
	v_or_b32_e32 v56, v49, v186
	v_min_i32_e32 v56, v56, v50
	v_cndmask_b32_e64 v54, 0, 1, vcc
	v_cmp_ge_i32_e32 vcc, v53, v31
	v_or_b32_e32 v59, 0x80, v49
	v_or_b32_e32 v60, v59, v1
	v_cndmask_b32_e64 v55, 0, 1, vcc
	v_cmp_ge_i32_e32 vcc, v53, v32
	v_min_i32_e32 v60, v60, v50
	v_or_b32_e32 v59, v59, v186
	v_addc_co_u32_e32 v54, vcc, v54, v55, vcc
	v_cmp_ge_i32_e32 vcc, v53, v33
	v_min_i32_e32 v50, v59, v50
	s_ashr_i32 s3, s2, 31
	v_cndmask_b32_e64 v55, 0, 1, vcc
	v_cmp_ge_i32_e32 vcc, v53, v38
	s_lshl_b64 s[0:1], s[2:3], 23
	s_add_u32 s5, s52, s0
	v_addc_co_u32_e32 v54, vcc, v54, v55, vcc
	v_cmp_ge_i32_e32 vcc, v53, v39
	s_addc_u32 s23, s53, s1
	s_lshl_b64 s[2:3], s[2:3], 15
	v_cndmask_b32_e64 v55, 0, 1, vcc
	v_cmp_ge_i32_e32 vcc, v53, v40
	s_add_u32 s2, s46, s2
	s_addc_u32 s3, s47, s3
	v_addc_co_u32_e32 v54, vcc, v54, v55, vcc
	v_cmp_ge_i32_e32 vcc, v53, v41
	s_lshl_b32 s64, s4, 8
	s_nop 0
	v_cndmask_b32_e64 v55, 0, 1, vcc
	v_cmp_ge_i32_e32 vcc, v53, v42
	s_nop 1
	v_addc_co_u32_e32 v54, vcc, v54, v55, vcc
	v_cmp_ge_i32_e32 vcc, v53, v43
	s_nop 1
	v_cndmask_b32_e64 v55, 0, 1, vcc
	v_cmp_ge_i32_e32 vcc, v53, v44
	s_nop 1
	v_addc_co_u32_e32 v54, vcc, v54, v55, vcc
	v_cmp_ge_i32_e32 vcc, v53, v45
	s_nop 1
	v_cndmask_b32_e64 v55, 0, 1, vcc
	v_cmp_ge_i32_e32 vcc, v53, v46
	s_nop 1
	v_addc_co_u32_e32 v54, vcc, v54, v55, vcc
	v_cmp_ge_i32_e32 vcc, v53, v47
	s_nop 1
	v_cndmask_b32_e64 v55, 0, 1, vcc
	v_cmp_ge_i32_e32 vcc, v53, v52
	s_nop 1
	v_addc_co_u32_e32 v54, vcc, v54, v55, vcc
	v_cmp_ge_i32_e32 vcc, v56, v30
	v_lshl_add_u32 v55, v54, 2, v51
	ds_read_b32 v55, v55
	v_cndmask_b32_e64 v57, 0, 1, vcc
	v_cmp_ge_i32_e32 vcc, v56, v31
	s_nop 1
	v_cndmask_b32_e64 v58, 0, 1, vcc
	v_cmp_ge_i32_e32 vcc, v56, v32
	s_nop 1
	v_addc_co_u32_e32 v57, vcc, v57, v58, vcc
	v_cmp_ge_i32_e32 vcc, v56, v33
	s_nop 1
	v_cndmask_b32_e64 v58, 0, 1, vcc
	v_cmp_ge_i32_e32 vcc, v56, v38
	s_nop 1
	v_addc_co_u32_e32 v57, vcc, v57, v58, vcc
	v_cmp_ge_i32_e32 vcc, v56, v39
	s_nop 1
	v_cndmask_b32_e64 v58, 0, 1, vcc
	v_cmp_ge_i32_e32 vcc, v56, v40
	s_nop 1
	v_addc_co_u32_e32 v57, vcc, v57, v58, vcc
	v_cmp_ge_i32_e32 vcc, v56, v41
	s_nop 1
	v_cndmask_b32_e64 v58, 0, 1, vcc
	v_cmp_ge_i32_e32 vcc, v56, v42
	s_nop 1
	v_addc_co_u32_e32 v57, vcc, v57, v58, vcc
	v_cmp_ge_i32_e32 vcc, v56, v43
	s_nop 1
	v_cndmask_b32_e64 v58, 0, 1, vcc
	v_cmp_ge_i32_e32 vcc, v56, v44
	s_nop 1
	v_addc_co_u32_e32 v57, vcc, v57, v58, vcc
	v_cmp_ge_i32_e32 vcc, v56, v45
	s_nop 1
	v_cndmask_b32_e64 v58, 0, 1, vcc
	v_cmp_ge_i32_e32 vcc, v56, v46
	s_nop 1
	v_addc_co_u32_e32 v57, vcc, v57, v58, vcc
	v_cmp_ge_i32_e32 vcc, v56, v47
	s_nop 1
	v_cndmask_b32_e64 v58, 0, 1, vcc
	v_cmp_ge_i32_e32 vcc, v56, v52
	s_nop 1
	v_addc_co_u32_e32 v57, vcc, v57, v58, vcc
	v_cmp_ge_i32_e32 vcc, v60, v30
	v_lshl_add_u32 v58, v57, 2, v51
	s_nop 0
	v_cndmask_b32_e64 v61, 0, 1, vcc
	v_cmp_ge_i32_e32 vcc, v60, v31
	s_nop 1
	v_cndmask_b32_e64 v62, 0, 1, vcc
	v_cmp_ge_i32_e32 vcc, v60, v32
	s_nop 1
	v_addc_co_u32_e32 v61, vcc, v61, v62, vcc
	v_cmp_ge_i32_e32 vcc, v60, v33
	s_nop 1
	v_cndmask_b32_e64 v62, 0, 1, vcc
	v_cmp_ge_i32_e32 vcc, v60, v38
	s_nop 1
	v_addc_co_u32_e32 v61, vcc, v61, v62, vcc
	v_cmp_ge_i32_e32 vcc, v60, v39
	s_nop 1
	v_cndmask_b32_e64 v62, 0, 1, vcc
	v_cmp_ge_i32_e32 vcc, v60, v40
	s_nop 1
	v_addc_co_u32_e32 v61, vcc, v61, v62, vcc
	v_cmp_ge_i32_e32 vcc, v60, v41
	s_nop 1
	v_cndmask_b32_e64 v62, 0, 1, vcc
	v_cmp_ge_i32_e32 vcc, v60, v42
	s_nop 1
	v_addc_co_u32_e32 v61, vcc, v61, v62, vcc
	v_cmp_ge_i32_e32 vcc, v60, v43
	s_nop 1
	v_cndmask_b32_e64 v62, 0, 1, vcc
	v_cmp_ge_i32_e32 vcc, v60, v44
	s_nop 1
	v_addc_co_u32_e32 v61, vcc, v61, v62, vcc
	v_cmp_ge_i32_e32 vcc, v60, v45
	s_nop 1
	v_cndmask_b32_e64 v62, 0, 1, vcc
	v_cmp_ge_i32_e32 vcc, v60, v46
	s_nop 1
	v_addc_co_u32_e32 v61, vcc, v61, v62, vcc
	v_cmp_ge_i32_e32 vcc, v60, v47
	s_nop 1
	v_cndmask_b32_e64 v62, 0, 1, vcc
	v_cmp_ge_i32_e32 vcc, v60, v52
	s_nop 1
	v_addc_co_u32_e32 v61, vcc, v61, v62, vcc
	v_cmp_ge_i32_e32 vcc, v50, v30
	v_lshl_add_u32 v62, v61, 2, v51
	s_nop 0
	v_cndmask_b32_e64 v30, 0, 1, vcc
	v_cmp_ge_i32_e32 vcc, v50, v31
	s_nop 1
	v_cndmask_b32_e64 v31, 0, 1, vcc
	v_cmp_ge_i32_e32 vcc, v50, v32
	s_nop 1
	v_addc_co_u32_e32 v30, vcc, v30, v31, vcc
	v_cmp_ge_i32_e32 vcc, v50, v33
	s_nop 1
	v_cndmask_b32_e64 v31, 0, 1, vcc
	v_cmp_ge_i32_e32 vcc, v50, v38
	s_nop 1
	v_addc_co_u32_e32 v30, vcc, v30, v31, vcc
	v_cmp_ge_i32_e32 vcc, v50, v39
	s_nop 1
	v_cndmask_b32_e64 v31, 0, 1, vcc
	v_cmp_ge_i32_e32 vcc, v50, v40
	s_nop 1
	v_addc_co_u32_e32 v30, vcc, v30, v31, vcc
	v_cmp_ge_i32_e32 vcc, v50, v41
	s_nop 1
	v_cndmask_b32_e64 v31, 0, 1, vcc
	v_cmp_ge_i32_e32 vcc, v50, v42
	s_nop 1
	v_addc_co_u32_e32 v30, vcc, v30, v31, vcc
	v_cmp_ge_i32_e32 vcc, v50, v43
	s_nop 1
	v_cndmask_b32_e64 v31, 0, 1, vcc
	v_cmp_ge_i32_e32 vcc, v50, v44
	s_nop 1
	v_addc_co_u32_e32 v30, vcc, v30, v31, vcc
	v_cmp_ge_i32_e32 vcc, v50, v45
	s_nop 1
	v_cndmask_b32_e64 v31, 0, 1, vcc
	v_cmp_ge_i32_e32 vcc, v50, v46
	s_nop 1
	v_addc_co_u32_e32 v30, vcc, v30, v31, vcc
	v_cmp_ge_i32_e32 vcc, v50, v47
	s_nop 1
	v_cndmask_b32_e64 v31, 0, 1, vcc
	v_cmp_ge_i32_e32 vcc, v50, v52
	s_nop 1
	v_addc_co_u32_e32 v40, vcc, v30, v31, vcc
	v_lshl_add_u32 v30, v40, 2, v51
	ds_read_b32 v32, v58
	ds_read_b32 v38, v62
	ds_read_b32 v41, v30
	s_waitcnt lgkmcnt(0)
	v_sub_u32_e32 v30, v53, v55
	v_lshl_add_u32 v30, v54, 9, v30
	v_sub_u32_e32 v32, v56, v32
	v_lshl_add_u32 v32, v57, 9, v32
	v_sub_u32_e32 v38, v60, v38
	v_lshl_add_u32 v40, v40, 9, v50
	v_ashrrev_i32_e32 v31, 31, v30
	v_ashrrev_i32_e32 v33, 31, v32
	v_lshl_add_u32 v38, v61, 9, v38
	v_sub_u32_e32 v40, v40, v41
	v_lshl_add_u64 v[30:31], v[30:31], 2, s[2:3]
	v_lshl_add_u64 v[32:33], v[32:33], 2, s[2:3]
	v_ashrrev_i32_e32 v39, 31, v38
	v_ashrrev_i32_e32 v41, 31, v40
	v_lshl_add_u64 v[38:39], v[38:39], 2, s[2:3]
	v_lshl_add_u64 v[40:41], v[40:41], 2, s[2:3]
	global_load_dword v30, v[30:31], off
	s_nop 0
	global_load_dword v31, v[32:33], off
	s_nop 0
	global_load_dword v32, v[38:39], off
	global_load_dword v33, v[40:41], off
	s_add_u32 s2, s26, s0
	s_addc_u32 s3, s27, s1
	s_lshl_b64 s[0:1], s[16:17], 9
	s_add_u32 s20, s2, s0
	v_sub_u32_e32 v38, v48, v49
	s_addc_u32 s21, s3, s1
	v_cmp_gt_i32_e32 vcc, s61, v38
	s_add_u32 s22, s5, s0
	s_addc_u32 s23, s23, s1
	v_cndmask_b32_e64 v208, 0, 1, vcc
	s_waitcnt vmcnt(0)
	v_lshl_or_b32 v209, v30, 12, v187
	v_lshl_or_b32 v210, v31, 12, v187
	v_lshl_or_b32 v211, v32, 12, v187
	v_lshl_or_b32 v212, v33, 12, v187

.LBB0_730:
	s_add_i32 s38, s4, 2
	s_cmp_eq_u32 s34, 28
	s_cselect_b64 s[4:5], -1, 0
	s_and_b64 s[34:35], s[4:5], exec
	s_cselect_b32 s38, 0, s38
	s_cselect_b32 s34, s23, s37
	s_cselect_b32 s35, s22, s36
	s_cselect_b32 s66, s21, s25
	s_cselect_b32 s67, s20, s24
	s_cselect_b32 s101, s100, s99
	s_cmp_lg_u64 s[2:3], 0
	s_cbranch_scc1 .Lw2_guE
	s_waitcnt vmcnt(4)
	s_branch .Lwd_guE

.Lwd_guE:
	v_cvt_pk_bf16_f32 v2, v2, v3
	v_cvt_pk_bf16_f32 v3, v4, v5
	s_ashr_i32 s39, s38, 31
	ds_write_b64 v199, v[2:3]
	v_cvt_pk_bf16_f32 v2, v6, v7
	v_cvt_pk_bf16_f32 v3, v8, v9
	s_lshl_b64 s[40:41], s[38:39], 18
	ds_write_b64 v200, v[2:3]
	v_cvt_pk_bf16_f32 v2, v10, v11
	v_cvt_pk_bf16_f32 v3, v12, v13
	s_add_u32 s68, s67, s40
	ds_write_b64 v201, v[2:3]
	v_cvt_pk_bf16_f32 v2, v14, v15
	v_cvt_pk_bf16_f32 v3, v16, v17
	s_addc_u32 s69, s66, s41
	ds_write_b64 v202, v[2:3]
	v_cvt_pk_bf16_f32 v2, v18, v19
	v_cvt_pk_bf16_f32 v3, v20, v21
	s_add_u32 s40, s35, s40
	ds_write_b64 v203, v[2:3]
	v_cvt_pk_bf16_f32 v2, v22, v23
	v_cvt_pk_bf16_f32 v3, v24, v25
	s_addc_u32 s41, s34, s41
	ds_write_b64 v204, v[2:3]
	v_cvt_pk_bf16_f32 v2, v26, v27
	v_cvt_pk_bf16_f32 v3, v28, v29
	s_add_u32 s70, s68, 0x2000
	ds_write_b64 v205, v[2:3]
	v_cvt_pk_bf16_f32 v2, v34, v35
	v_cvt_pk_bf16_f32 v3, v36, v37
	ds_write_b64 v206, v[2:3]
	s_addc_u32 s71, s69, 0
	s_cmp_lg_u32 s101, 0
	s_cbranch_scc1 .Lrot_guE
	global_load_dwordx4 v[34:37], v189, s[68:69]
	global_load_dwordx4 v[22:25], v189, s[40:41]
	s_add_u32 s70, s68, 0x2000
	s_addc_u32 s71, s69, 0
	s_add_u32 s72, s40, 0x2000
	s_addc_u32 s73, s41, 0
	global_load_dwordx4 v[26:29], v189, s[70:71]
	global_load_dwordx4 v[14:17], v189, s[72:73]
	s_add_u32 s70, s68, 0x4000
	s_addc_u32 s71, s69, 0
	s_add_u32 s72, s40, 0x4000
	s_addc_u32 s73, s41, 0
	global_load_dwordx4 v[18:21], v189, s[70:71]
	global_load_dwordx4 v[6:9], v189, s[72:73]
	s_add_u32 s70, s68, 0x6000
	s_addc_u32 s71, s69, 0
	s_add_u32 s72, s40, 0x6000
	s_addc_u32 s73, s41, 0
	global_load_dwordx4 v[10:13], v189, s[70:71]
	global_load_dwordx4 v[2:5], v189, s[72:73]
	s_branch .Lrotd_guE
.Lrot_guE:
	s_add_u32 s70, s68, 0x4000
	s_addc_u32 s71, s69, 0
	s_add_u32 s72, s40, 0x4000
	s_addc_u32 s73, s41, 0
	global_load_dwordx4 v[18:21], v189, s[70:71]
	global_load_dwordx4 v[6:9], v189, s[72:73]
	s_add_u32 s70, s68, 0x6000
	s_addc_u32 s71, s69, 0
	s_add_u32 s72, s40, 0x6000
	s_addc_u32 s73, s41, 0
	global_load_dwordx4 v[10:13], v189, s[70:71]
	global_load_dwordx4 v[2:5], v189, s[72:73]
	global_load_dwordx4 v[34:37], v189, s[68:69]
	global_load_dwordx4 v[22:25], v189, s[40:41]
	s_add_u32 s70, s68, 0x2000
	s_addc_u32 s71, s69, 0
	s_add_u32 s72, s40, 0x2000
	s_addc_u32 s73, s41, 0
	global_load_dwordx4 v[26:29], v189, s[70:71]
	global_load_dwordx4 v[14:17], v189, s[72:73]
.Lrotd_guE:
	s_lshl_b64 s[40:41], s[38:39], 7
	s_add_u32 s40, s8, s40
	s_mov_b32 m0, s51
	s_waitcnt vmcnt(8)
	s_waitcnt lgkmcnt(0)
	s_barrier
	s_addc_u32 s41, s9, s41
	v_cndmask_b32_e64 v164, v178, v209, s[4:5]
	v_cndmask_b32_e64 v163, v180, v210, s[4:5]
	global_load_lds_dwordx4 v164, s[40:41]
	s_mov_b32 m0, s60
	v_cndmask_b32_e64 v162, v213, v208, s[4:5]
	global_load_lds_dwordx4 v163, s[40:41]
	v_cmp_ne_u32_e32 vcc, 0, v162
	s_mov_b64 s[96:97], vcc
	s_cbranch_vccnz .LBB0_732
	v_cndmask_b32_e64 v163, v182, v211, s[4:5]
	s_add_i32 m0, s51, 0x4000
	v_cndmask_b32_e64 v162, v184, v212, s[4:5]
	global_load_lds_dwordx4 v163, s[40:41]
	s_add_i32 m0, s51, 0x6000
	s_nop 0
	global_load_lds_dwordx4 v162, s[40:41]

.Lwd_guO:
	v_cvt_pk_bf16_f32 v34, v34, v35
	v_cvt_pk_bf16_f32 v35, v36, v37
	ds_write_b64 v194, v[34:35]
	v_cvt_pk_bf16_f32 v22, v22, v23
	v_cvt_pk_bf16_f32 v23, v24, v25
	s_add_u32 s4, s35, s4
	ds_write_b64 v194, v[22:23] offset:16384
	v_cvt_pk_bf16_f32 v22, v26, v27
	v_cvt_pk_bf16_f32 v23, v28, v29
	ds_write_b64 v195, v[22:23]
	v_cvt_pk_bf16_f32 v14, v14, v15
	v_cvt_pk_bf16_f32 v15, v16, v17
	s_addc_u32 s5, s34, s5
	ds_write_b64 v195, v[14:15] offset:16384
	v_cvt_pk_bf16_f32 v14, v18, v19
	v_cvt_pk_bf16_f32 v15, v20, v21
	ds_write_b64 v196, v[14:15]
	v_cvt_pk_bf16_f32 v6, v6, v7
	v_cvt_pk_bf16_f32 v7, v8, v9
	s_add_u32 s34, s2, 0x2000
	ds_write_b64 v196, v[6:7] offset:16384
	v_cvt_pk_bf16_f32 v6, v10, v11
	v_cvt_pk_bf16_f32 v7, v12, v13
	ds_write_b64 v197, v[6:7]
	v_cvt_pk_bf16_f32 v2, v2, v3
	v_cvt_pk_bf16_f32 v3, v4, v5
	ds_write_b64 v197, v[2:3] offset:16384
	s_addc_u32 s35, s3, 0
	s_cmp_lg_u32 s101, 0
	s_cbranch_scc1 .Lrot_guO
	global_load_dwordx4 v[2:5], v189, s[2:3]
	global_load_dwordx4 v[6:9], v189, s[4:5]
	s_add_u32 s34, s2, 0x2000
	s_addc_u32 s35, s3, 0
	s_add_u32 s38, s4, 0x2000
	s_addc_u32 s39, s5, 0
	global_load_dwordx4 v[10:13], v189, s[34:35]
	global_load_dwordx4 v[14:17], v189, s[38:39]
	s_add_u32 s34, s2, 0x4000
	s_addc_u32 s35, s3, 0
	s_add_u32 s38, s4, 0x4000
	s_addc_u32 s39, s5, 0
	global_load_dwordx4 v[18:21], v189, s[34:35]
	global_load_dwordx4 v[22:25], v189, s[38:39]
	s_add_u32 s34, s2, 0x6000
	s_addc_u32 s35, s3, 0
	s_add_u32 s38, s4, 0x6000
	s_addc_u32 s39, s5, 0
	global_load_dwordx4 v[26:29], v189, s[34:35]
	global_load_dwordx4 v[34:37], v189, s[38:39]
	s_branch .Lrotd_guO
.Lrot_guO:
	s_add_u32 s34, s2, 0x4000
	s_addc_u32 s35, s3, 0
	s_add_u32 s38, s4, 0x4000
	s_addc_u32 s39, s5, 0
	global_load_dwordx4 v[18:21], v189, s[34:35]
	global_load_dwordx4 v[22:25], v189, s[38:39]
	s_add_u32 s34, s2, 0x6000
	s_addc_u32 s35, s3, 0
	s_add_u32 s38, s4, 0x6000
	s_addc_u32 s39, s5, 0
	global_load_dwordx4 v[26:29], v189, s[34:35]
	global_load_dwordx4 v[34:37], v189, s[38:39]
	global_load_dwordx4 v[2:5], v189, s[2:3]
	global_load_dwordx4 v[6:9], v189, s[4:5]
	s_add_u32 s34, s2, 0x2000
	s_addc_u32 s35, s3, 0
	s_add_u32 s38, s4, 0x2000
	s_addc_u32 s39, s5, 0
	global_load_dwordx4 v[10:13], v189, s[34:35]
	global_load_dwordx4 v[14:17], v189, s[38:39]
.Lrotd_guO:
	s_waitcnt vmcnt(8)
	s_waitcnt lgkmcnt(0)
	s_barrier
	s_cmp_gt_u32 s17, 29
	s_cbranch_scc1 .LBB0_738
	s_mov_b32 s34, s17
	s_branch .LBB0_724
.LBB0_738:
	v_mul_f32_e32 v162, 0xbfb8aa3b, v158
	v_exp_f32_e32 v163, v162
	v_mul_f32_e32 v162, 0xbfb8aa3b, v159
	v_exp_f32_e32 v165, v162
	v_add_u32_e32 v162, s65, v188
	v_add_f32_e32 v163, 1.0, v163
	v_rcp_f32_e32 v163, v163
	v_add_f32_e32 v165, 1.0, v165
	v_rcp_f32_e32 v166, v165
	v_lshl_or_b32 v164, s18, 7, v198
	v_mul_f32_e32 v158, v158, v163
	v_mul_f32_e32 v150, v158, v150
	v_mul_f32_e32 v158, v159, v166
	v_mul_f32_e32 v159, 0xbfb8aa3b, v160
	v_exp_f32_e32 v159, v159
	v_mul_f32_e32 v163, 0xbfb8aa3b, v161
	v_exp_f32_e32 v163, v163
	v_mul_f32_e32 v151, v158, v151
	v_add_f32_e32 v158, 1.0, v159
	v_rcp_f32_e32 v158, v158
	v_add_f32_e32 v159, 1.0, v163
	v_rcp_f32_e32 v159, v159
	v_cvt_pk_bf16_f32 v150, v150, v151
	v_mul_f32_e32 v151, v160, v158
	v_mul_f32_e32 v158, 0xbfb8aa3b, v154
	v_exp_f32_e32 v158, v158
	v_mul_f32_e32 v151, v151, v152
	v_mul_f32_e32 v152, v161, v159
	v_mul_f32_e32 v159, 0xbfb8aa3b, v155
	v_exp_f32_e32 v159, v159
	v_mul_f32_e32 v152, v152, v153
	v_add_f32_e32 v153, 1.0, v158
	v_rcp_f32_e32 v153, v153
	v_add_f32_e32 v158, 1.0, v159
	v_rcp_f32_e32 v158, v158
	v_cvt_pk_bf16_f32 v151, v151, v152
	v_mul_f32_e32 v152, v154, v153
	v_mul_f32_e32 v153, 0xbfb8aa3b, v156
	v_exp_f32_e32 v153, v153
	v_mul_f32_e32 v154, 0xbfb8aa3b, v157
	v_exp_f32_e32 v154, v154
	v_mul_f32_e32 v142, v152, v142
	v_mul_f32_e32 v152, v155, v158
	v_mul_f32_e32 v143, v152, v143
	v_add_f32_e32 v152, 1.0, v153
	v_rcp_f32_e32 v153, v152
	v_add_f32_e32 v152, 1.0, v154
	v_rcp_f32_e32 v154, v152
	v_cvt_pk_bf16_f32 v152, v142, v143
	v_mul_f32_e32 v155, 0xbfb8aa3b, v147
	v_exp_f32_e32 v155, v155
	v_mul_f32_e32 v143, v157, v154
	v_mul_f32_e32 v154, 0xbfb8aa3b, v146
	v_exp_f32_e32 v154, v154
	v_add_f32_e32 v155, 1.0, v155
	v_rcp_f32_e32 v155, v155
	v_mul_f32_e32 v142, v156, v153
	v_add_f32_e32 v154, 1.0, v154
	v_rcp_f32_e32 v154, v154
	v_mul_f32_e32 v142, v142, v144
	v_mul_f32_e32 v143, v143, v145
	v_ashrrev_i32_e32 v163, 31, v162
	v_mul_f32_e32 v146, v146, v154
	v_mul_f32_e32 v134, v146, v134
	v_mul_f32_e32 v146, v147, v155
	v_mul_f32_e32 v147, 0xbfb8aa3b, v148
	v_ashrrev_i32_e32 v165, 31, v164
	v_cvt_pk_bf16_f32 v153, v142, v143
	v_lshlrev_b64 v[142:143], 11, v[162:163]
	v_exp_f32_e32 v147, v147
	v_lshl_add_u64 v[142:143], s[12:13], 0, v[142:143]
	v_lshlrev_b64 v[144:145], 1, v[164:165]
	v_permlane16_swap_b32_e32 v150, v152
	v_permlane16_swap_b32_e32 v151, v153
	v_lshl_add_u64 v[142:143], v[142:143], 0, v[144:145]
	global_store_dwordx4 v[142:143], v[150:153], off
	v_mul_f32_e32 v135, v146, v135
	v_add_f32_e32 v146, 1.0, v147
	v_mul_f32_e32 v150, 0xbfb8aa3b, v149
	v_exp_f32_e32 v150, v150
	v_rcp_f32_e32 v146, v146
	v_cvt_pk_bf16_f32 v134, v134, v135
	v_add_f32_e32 v147, 1.0, v150
	v_rcp_f32_e32 v147, v147
	v_mul_f32_e32 v135, v148, v146
	v_mul_f32_e32 v146, 0xbfb8aa3b, v138
	v_exp_f32_e32 v146, v146
	v_mul_f32_e32 v135, v135, v136
	v_mul_f32_e32 v136, v149, v147
	v_mul_f32_e32 v147, 0xbfb8aa3b, v139
	v_exp_f32_e32 v147, v147
	v_mul_f32_e32 v136, v136, v137
	v_add_f32_e32 v137, 1.0, v146
	v_rcp_f32_e32 v137, v137
	v_add_f32_e32 v146, 1.0, v147
	v_rcp_f32_e32 v146, v146
	v_cvt_pk_bf16_f32 v135, v135, v136
	v_mul_f32_e32 v136, v138, v137
	v_mul_f32_e32 v137, 0xbfb8aa3b, v140
	v_exp_f32_e32 v137, v137
	v_mul_f32_e32 v138, 0xbfb8aa3b, v141
	v_exp_f32_e32 v138, v138
	v_mul_f32_e32 v126, v136, v126
	v_mul_f32_e32 v136, v139, v146
	v_mul_f32_e32 v127, v136, v127
	v_add_f32_e32 v136, 1.0, v137
	v_rcp_f32_e32 v137, v136
	v_add_f32_e32 v136, 1.0, v138
	v_rcp_f32_e32 v138, v136
	v_cvt_pk_bf16_f32 v136, v126, v127
	v_mul_f32_e32 v126, v140, v137
	v_mul_f32_e32 v126, v126, v128
	v_mul_f32_e32 v127, v141, v138
	v_mul_f32_e32 v128, 0xbfb8aa3b, v130
	v_mul_f32_e32 v127, v127, v129
	v_exp_f32_e32 v128, v128
	v_mul_f32_e32 v129, 0xbfb8aa3b, v131
	v_cvt_pk_bf16_f32 v137, v126, v127
	v_or_b32_e32 v126, 16, v162
	v_exp_f32_e32 v129, v129
	v_ashrrev_i32_e32 v127, 31, v126
	v_lshlrev_b64 v[126:127], 11, v[126:127]
	v_lshl_add_u64 v[126:127], s[12:13], 0, v[126:127]
	v_add_f32_e32 v128, 1.0, v128
	v_permlane16_swap_b32_e32 v134, v136
	v_permlane16_swap_b32_e32 v135, v137
	v_lshl_add_u64 v[126:127], v[126:127], 0, v[144:145]
	v_rcp_f32_e32 v128, v128
	v_add_f32_e32 v129, 1.0, v129
	v_rcp_f32_e32 v129, v129
	global_store_dwordx4 v[126:127], v[134:137], off
	v_mul_f32_e32 v127, 0xbfb8aa3b, v132
	v_exp_f32_e32 v127, v127
	v_mul_f32_e32 v126, v130, v128
	v_mul_f32_e32 v118, v126, v118
	v_mul_f32_e32 v126, v131, v129
	v_mul_f32_e32 v128, 0xbfb8aa3b, v133
	v_exp_f32_e32 v128, v128
	v_mul_f32_e32 v119, v126, v119
	v_add_f32_e32 v126, 1.0, v127
	v_rcp_f32_e32 v126, v126
	v_add_f32_e32 v127, 1.0, v128
	v_rcp_f32_e32 v127, v127
	v_cvt_pk_bf16_f32 v118, v118, v119
	v_mul_f32_e32 v119, v132, v126
	v_mul_f32_e32 v126, 0xbfb8aa3b, v122
	v_exp_f32_e32 v126, v126
	v_mul_f32_e32 v119, v119, v120
	v_mul_f32_e32 v120, v133, v127
	v_mul_f32_e32 v127, 0xbfb8aa3b, v123
	v_exp_f32_e32 v127, v127
	v_mul_f32_e32 v120, v120, v121
	v_add_f32_e32 v121, 1.0, v126
	v_rcp_f32_e32 v121, v121
	v_add_f32_e32 v126, 1.0, v127
	v_rcp_f32_e32 v126, v126
	v_cvt_pk_bf16_f32 v119, v119, v120
	v_mul_f32_e32 v120, v122, v121
	v_mul_f32_e32 v121, 0xbfb8aa3b, v124
	v_exp_f32_e32 v121, v121
	v_mul_f32_e32 v122, 0xbfb8aa3b, v125
	v_exp_f32_e32 v122, v122
	v_mul_f32_e32 v110, v120, v110
	v_mul_f32_e32 v120, v123, v126
	v_mul_f32_e32 v111, v120, v111
	v_add_f32_e32 v120, 1.0, v121
	v_rcp_f32_e32 v121, v120
	v_add_f32_e32 v120, 1.0, v122
	v_rcp_f32_e32 v122, v120
	v_cvt_pk_bf16_f32 v120, v110, v111
	v_mul_f32_e32 v110, v124, v121
	v_mul_f32_e32 v110, v110, v112
	v_mul_f32_e32 v111, v125, v122
	v_mul_f32_e32 v112, 0xbfb8aa3b, v114
	v_mul_f32_e32 v111, v111, v113
	v_exp_f32_e32 v112, v112
	v_mul_f32_e32 v113, 0xbfb8aa3b, v115
	v_cvt_pk_bf16_f32 v121, v110, v111
	v_or_b32_e32 v110, 32, v162
	v_exp_f32_e32 v113, v113
	v_ashrrev_i32_e32 v111, 31, v110
	v_lshlrev_b64 v[110:111], 11, v[110:111]
	v_lshl_add_u64 v[110:111], s[12:13], 0, v[110:111]
	v_add_f32_e32 v112, 1.0, v112
	v_permlane16_swap_b32_e32 v118, v120
	v_permlane16_swap_b32_e32 v119, v121
	v_lshl_add_u64 v[110:111], v[110:111], 0, v[144:145]
	v_rcp_f32_e32 v112, v112
	v_add_f32_e32 v113, 1.0, v113
	v_rcp_f32_e32 v113, v113
	global_store_dwordx4 v[110:111], v[118:121], off
	v_mul_f32_e32 v111, 0xbfb8aa3b, v116
	v_exp_f32_e32 v111, v111
	v_mul_f32_e32 v110, v114, v112
	v_mul_f32_e32 v102, v110, v102
	v_mul_f32_e32 v110, v115, v113
	v_mul_f32_e32 v112, 0xbfb8aa3b, v117
	v_exp_f32_e32 v112, v112
	v_mul_f32_e32 v103, v110, v103
	v_add_f32_e32 v110, 1.0, v111
	v_rcp_f32_e32 v110, v110
	v_add_f32_e32 v111, 1.0, v112
	v_rcp_f32_e32 v111, v111
	v_cvt_pk_bf16_f32 v102, v102, v103
	v_mul_f32_e32 v103, v116, v110
	v_mul_f32_e32 v110, 0xbfb8aa3b, v106
	v_exp_f32_e32 v110, v110
	v_mul_f32_e32 v103, v103, v104
	v_mul_f32_e32 v104, v117, v111
	v_mul_f32_e32 v111, 0xbfb8aa3b, v107
	v_exp_f32_e32 v111, v111
	v_mul_f32_e32 v104, v104, v105
	v_add_f32_e32 v105, 1.0, v110
	v_rcp_f32_e32 v105, v105
	v_add_f32_e32 v110, 1.0, v111
	v_rcp_f32_e32 v110, v110
	v_cvt_pk_bf16_f32 v103, v103, v104
	v_mul_f32_e32 v104, v106, v105
	v_mul_f32_e32 v105, 0xbfb8aa3b, v108
	v_exp_f32_e32 v105, v105
	v_mul_f32_e32 v106, 0xbfb8aa3b, v109
	v_exp_f32_e32 v106, v106
	v_mul_f32_e32 v98, v104, v98
	v_mul_f32_e32 v104, v107, v110
	v_mul_f32_e32 v99, v104, v99
	v_add_f32_e32 v104, 1.0, v105
	v_rcp_f32_e32 v105, v104
	v_add_f32_e32 v104, 1.0, v106
	v_rcp_f32_e32 v106, v104
	v_cvt_pk_bf16_f32 v104, v98, v99
	v_mul_f32_e32 v98, v108, v105
	v_mul_f32_e32 v98, v98, v100
	v_mul_f32_e32 v99, v109, v106
	v_mul_f32_e32 v100, 0xbfb8aa3b, v94
	v_mul_f32_e32 v99, v99, v101
	v_exp_f32_e32 v100, v100
	v_mul_f32_e32 v101, 0xbfb8aa3b, v95
	v_exp_f32_e32 v101, v101
	v_cvt_pk_bf16_f32 v105, v98, v99
	v_add_f32_e32 v100, 1.0, v100
	v_rcp_f32_e32 v100, v100
	v_add_f32_e32 v101, 1.0, v101
	v_or_b32_e32 v98, 48, v162
	v_rcp_f32_e32 v101, v101
	v_ashrrev_i32_e32 v99, 31, v98
	v_lshlrev_b64 v[98:99], 11, v[98:99]
	v_lshl_add_u64 v[98:99], s[12:13], 0, v[98:99]
	v_mul_f32_e32 v94, v94, v100
	v_permlane16_swap_b32_e32 v102, v104
	v_permlane16_swap_b32_e32 v103, v105
	v_lshl_add_u64 v[98:99], v[98:99], 0, v[144:145]
	v_mul_f32_e32 v90, v94, v90
	v_mul_f32_e32 v94, v95, v101
	v_mul_f32_e32 v95, 0xbfb8aa3b, v96
	global_store_dwordx4 v[98:99], v[102:105], off
	v_exp_f32_e32 v95, v95
	v_mul_f32_e32 v98, 0xbfb8aa3b, v97
	v_exp_f32_e32 v98, v98
	v_mul_f32_e32 v91, v94, v91
	v_add_f32_e32 v94, 1.0, v95
	v_rcp_f32_e32 v94, v94
	v_add_f32_e32 v95, 1.0, v98
	v_rcp_f32_e32 v95, v95
	v_cvt_pk_bf16_f32 v90, v90, v91
	v_mul_f32_e32 v91, v96, v94
	v_mul_f32_e32 v94, 0xbfb8aa3b, v86
	v_mul_f32_e32 v91, v91, v92
	v_mul_f32_e32 v92, v97, v95
	v_exp_f32_e32 v94, v94
	v_mul_f32_e32 v95, 0xbfb8aa3b, v87
	v_exp_f32_e32 v95, v95
	v_mul_f32_e32 v92, v92, v93
	v_add_f32_e32 v93, 1.0, v94
	v_rcp_f32_e32 v93, v93
	v_add_f32_e32 v94, 1.0, v95
	v_rcp_f32_e32 v94, v94
	v_cvt_pk_bf16_f32 v91, v91, v92
	v_mul_f32_e32 v86, v86, v93
	v_mul_f32_e32 v82, v86, v82
	v_mul_f32_e32 v86, v87, v94
	v_mul_f32_e32 v87, 0xbfb8aa3b, v88
	v_exp_f32_e32 v87, v87
	v_mul_f32_e32 v92, 0xbfb8aa3b, v89
	v_exp_f32_e32 v92, v92
	v_mul_f32_e32 v83, v86, v83
	v_add_f32_e32 v86, 1.0, v87
	v_rcp_f32_e32 v86, v86
	v_add_f32_e32 v87, 1.0, v92
	v_rcp_f32_e32 v87, v87
	v_cvt_pk_bf16_f32 v92, v82, v83
	v_mul_f32_e32 v82, v88, v86
	v_mul_f32_e32 v82, v82, v84
	v_mul_f32_e32 v83, v89, v87
	v_mul_f32_e32 v83, v83, v85
	v_cvt_pk_bf16_f32 v93, v82, v83
	v_mul_f32_e32 v82, 0xbfb8aa3b, v78
	v_exp_f32_e32 v84, v82
	v_mul_f32_e32 v82, 0xbfb8aa3b, v79
	v_exp_f32_e32 v85, v82
	v_add_co_u32_e32 v82, vcc, s19, v142
	v_add_f32_e32 v84, 1.0, v84
	v_rcp_f32_e32 v84, v84
	v_add_f32_e32 v85, 1.0, v85
	v_rcp_f32_e32 v85, v85
	v_permlane16_swap_b32_e32 v90, v92
	v_mul_f32_e32 v78, v78, v84
	v_permlane16_swap_b32_e32 v91, v93
	v_addc_co_u32_e32 v83, vcc, 0, v143, vcc
	v_mul_f32_e32 v74, v78, v74
	v_mul_f32_e32 v78, v79, v85
	v_mul_f32_e32 v79, 0xbfb8aa3b, v80
	global_store_dwordx4 v[82:83], v[90:93], off
	v_exp_f32_e32 v79, v79
	v_mul_f32_e32 v82, 0xbfb8aa3b, v81
	v_exp_f32_e32 v82, v82
	v_mul_f32_e32 v75, v78, v75
	v_add_f32_e32 v78, 1.0, v79
	v_rcp_f32_e32 v78, v78
	v_add_f32_e32 v79, 1.0, v82
	v_rcp_f32_e32 v79, v79
	v_cvt_pk_bf16_f32 v74, v74, v75
	v_mul_f32_e32 v75, v80, v78
	v_mul_f32_e32 v78, 0xbfb8aa3b, v70
	v_mul_f32_e32 v75, v75, v76
	v_mul_f32_e32 v76, v81, v79
	v_exp_f32_e32 v78, v78
	v_mul_f32_e32 v79, 0xbfb8aa3b, v71
	v_exp_f32_e32 v79, v79
	v_mul_f32_e32 v76, v76, v77
	v_add_f32_e32 v77, 1.0, v78
	v_rcp_f32_e32 v77, v77
	v_add_f32_e32 v78, 1.0, v79
	v_rcp_f32_e32 v78, v78
	v_cvt_pk_bf16_f32 v75, v75, v76
	v_mul_f32_e32 v70, v70, v77
	v_mul_f32_e32 v66, v70, v66
	v_mul_f32_e32 v70, v71, v78
	v_mul_f32_e32 v71, 0xbfb8aa3b, v72
	v_exp_f32_e32 v71, v71
	v_mul_f32_e32 v76, 0xbfb8aa3b, v73
	v_exp_f32_e32 v76, v76
	v_mul_f32_e32 v67, v70, v67
	v_add_f32_e32 v70, 1.0, v71
	v_rcp_f32_e32 v70, v70
	v_add_f32_e32 v71, 1.0, v76
	v_rcp_f32_e32 v71, v71
	v_cvt_pk_bf16_f32 v76, v66, v67
	v_mul_f32_e32 v66, v72, v70
	v_mul_f32_e32 v66, v66, v68
	v_mul_f32_e32 v67, v73, v71
	v_mul_f32_e32 v67, v67, v69
	v_cvt_pk_bf16_f32 v77, v66, v67
	v_mul_f32_e32 v66, 0xbfb8aa3b, v62
	v_exp_f32_e32 v68, v66
	v_mul_f32_e32 v66, 0xbfb8aa3b, v63
	v_exp_f32_e32 v69, v66
	v_add_co_u32_e32 v66, vcc, s62, v142
	v_add_f32_e32 v68, 1.0, v68
	v_rcp_f32_e32 v68, v68
	v_add_f32_e32 v69, 1.0, v69
	v_rcp_f32_e32 v69, v69
	v_permlane16_swap_b32_e32 v74, v76
	v_mul_f32_e32 v62, v62, v68
	v_permlane16_swap_b32_e32 v75, v77
	v_addc_co_u32_e32 v67, vcc, 0, v143, vcc
	v_mul_f32_e32 v58, v62, v58
	v_mul_f32_e32 v62, v63, v69
	v_mul_f32_e32 v63, 0xbfb8aa3b, v64
	global_store_dwordx4 v[66:67], v[74:77], off
	v_exp_f32_e32 v63, v63
	v_mul_f32_e32 v66, 0xbfb8aa3b, v65
	v_exp_f32_e32 v66, v66
	v_mul_f32_e32 v59, v62, v59
	v_add_f32_e32 v62, 1.0, v63
	v_rcp_f32_e32 v62, v62
	v_add_f32_e32 v63, 1.0, v66
	v_rcp_f32_e32 v63, v63
	v_cvt_pk_bf16_f32 v58, v58, v59
	v_mul_f32_e32 v59, v64, v62
	v_mul_f32_e32 v62, 0xbfb8aa3b, v54
	v_mul_f32_e32 v59, v59, v60
	v_mul_f32_e32 v60, v65, v63
	v_exp_f32_e32 v62, v62
	v_mul_f32_e32 v63, 0xbfb8aa3b, v55
	v_exp_f32_e32 v63, v63
	v_mul_f32_e32 v60, v60, v61
	v_add_f32_e32 v61, 1.0, v62
	v_rcp_f32_e32 v61, v61
	v_add_f32_e32 v62, 1.0, v63
	v_rcp_f32_e32 v62, v62
	v_cvt_pk_bf16_f32 v59, v59, v60
	v_mul_f32_e32 v54, v54, v61
	v_mul_f32_e32 v50, v54, v50
	v_mul_f32_e32 v54, v55, v62
	v_mul_f32_e32 v55, 0xbfb8aa3b, v56
	v_exp_f32_e32 v55, v55
	v_mul_f32_e32 v60, 0xbfb8aa3b, v57
	v_exp_f32_e32 v60, v60
	v_mul_f32_e32 v51, v54, v51
	v_add_f32_e32 v54, 1.0, v55
	v_rcp_f32_e32 v54, v54
	v_add_f32_e32 v55, 1.0, v60
	v_rcp_f32_e32 v55, v55
	v_cvt_pk_bf16_f32 v60, v50, v51
	v_mul_f32_e32 v50, v56, v54
	v_mul_f32_e32 v50, v50, v52
	v_mul_f32_e32 v51, v57, v55
	v_mul_f32_e32 v51, v51, v53
	v_cvt_pk_bf16_f32 v61, v50, v51
	v_mul_f32_e32 v50, 0xbfb8aa3b, v46
	v_exp_f32_e32 v52, v50
	v_mul_f32_e32 v50, 0xbfb8aa3b, v47
	v_exp_f32_e32 v53, v50
	v_add_co_u32_e32 v50, vcc, s63, v142
	v_add_f32_e32 v52, 1.0, v52
	v_rcp_f32_e32 v52, v52
	v_add_f32_e32 v53, 1.0, v53
	v_rcp_f32_e32 v53, v53
	v_permlane16_swap_b32_e32 v58, v60
	v_mul_f32_e32 v46, v46, v52
	v_permlane16_swap_b32_e32 v59, v61
	v_addc_co_u32_e32 v51, vcc, 0, v143, vcc
	v_mul_f32_e32 v42, v46, v42
	v_mul_f32_e32 v46, v47, v53
	v_mul_f32_e32 v47, 0xbfb8aa3b, v48
	global_store_dwordx4 v[50:51], v[58:61], off
	v_exp_f32_e32 v47, v47
	v_mul_f32_e32 v50, 0xbfb8aa3b, v49
	v_exp_f32_e32 v50, v50
	v_mul_f32_e32 v43, v46, v43
	v_add_f32_e32 v46, 1.0, v47
	v_rcp_f32_e32 v46, v46
	v_add_f32_e32 v47, 1.0, v50
	v_rcp_f32_e32 v47, v47
	v_cvt_pk_bf16_f32 v42, v42, v43
	v_mul_f32_e32 v43, v48, v46
	v_mul_f32_e32 v46, 0xbfb8aa3b, v38
	v_mul_f32_e32 v43, v43, v44
	v_mul_f32_e32 v44, v49, v47
	v_exp_f32_e32 v46, v46
	v_mul_f32_e32 v47, 0xbfb8aa3b, v39
	v_exp_f32_e32 v47, v47
	v_mul_f32_e32 v44, v44, v45
	v_add_f32_e32 v45, 1.0, v46
	v_rcp_f32_e32 v45, v45
	v_add_f32_e32 v46, 1.0, v47
	v_rcp_f32_e32 v46, v46
	v_cvt_pk_bf16_f32 v43, v43, v44
	v_mul_f32_e32 v38, v38, v45
	v_mul_f32_e32 v30, v38, v30
	v_mul_f32_e32 v38, v39, v46
	v_mul_f32_e32 v39, 0xbfb8aa3b, v40
	v_exp_f32_e32 v39, v39
	v_mul_f32_e32 v44, 0xbfb8aa3b, v41
	v_exp_f32_e32 v44, v44
	v_mul_f32_e32 v31, v38, v31
	v_add_f32_e32 v38, 1.0, v39
	v_rcp_f32_e32 v38, v38
	v_add_f32_e32 v39, 1.0, v44
	v_rcp_f32_e32 v39, v39
	v_cvt_pk_bf16_f32 v44, v30, v31
	v_mul_f32_e32 v30, v40, v38
	v_mul_f32_e32 v30, v30, v32
	v_mul_f32_e32 v31, v41, v39
	v_mul_f32_e32 v31, v31, v33
	v_cvt_pk_bf16_f32 v45, v30, v31
	v_add_co_u32_e32 v30, vcc, 0x58000, v142
	v_permlane16_swap_b32_e32 v42, v44
	s_nop 0
	v_addc_co_u32_e32 v31, vcc, 0, v143, vcc
	v_permlane16_swap_b32_e32 v43, v45
	s_and_b64 vcc, exec, s[14:15]
	global_store_dwordx4 v[30:31], v[42:45], off
	s_cbranch_vccnz .LBB0_740
	v_mov_b32_e32 v178, v209
	v_mov_b32_e32 v180, v210
	v_mov_b32_e32 v182, v211
	v_mov_b32_e32 v184, v212
	v_mov_b32_e32 v213, v208
	s_mov_b32 s65, s64
	s_mov_b32 s18, s16
	s_mov_b64 s[36:37], s[22:23]
	s_mov_b32 s99, s100
	s_mov_b64 s[24:25], s[20:21]
	s_branch .LBB0_721

.LBB0_849:
	s_cmp_lt_i32 s76, s53
	s_cselect_b32 s61, s76, s60
	s_cmp_lt_i32 s61, 0
	s_cbranch_scc1 .LBB0_873
	s_add_u32 s62, s10, 0x1ed90000
	s_addc_u32 s63, s11, 0
	s_abs_i32 s64, s52
	v_cvt_f32_u32_e32 v4, s64
	s_sub_i32 s2, 0, s64
	s_abs_i32 s1, s61
	s_ashr_i32 s0, s61, 31
	v_rcp_iflag_f32_e32 v4, v4
	s_ashr_i32 s65, s52, 31
	s_lshr_b32 s9, s8, 6
	s_xor_b32 s0, s0, s65
	v_mul_f32_e32 v4, 0x4f7ffffe, v4
	v_cvt_u32_f32_e32 v4, v4
	v_lshlrev_b32_e32 v1, 4, v0
	v_and_b32_e32 v2, 32, v0
	v_bfe_u32 v3, v0, 2, 4
	v_readfirstlane_b32 s66, v4
	s_mul_i32 s2, s2, s66
	s_mul_hi_u32 s2, s66, s2
	s_add_i32 s66, s66, s2
	s_lshr_b32 s89, s61, 3
	s_lshl_b32 s89, s89, 2
	s_add_i32 s89, s89, 0x202e0
	v_mov_b32_e32 v222, s89
	ds_read_b32 v222, v222
	s_waitcnt lgkmcnt(0)
	v_lshlrev_b32_e32 v222, 2, v222
	v_add_u32_e32 v222, 0x20240, v222
	ds_read2_b32 v[252:253], v222 offset1:1
	s_waitcnt lgkmcnt(0)
	v_readfirstlane_b32 s90, v252
	v_readfirstlane_b32 s91, v253
	s_nop 3
	s_sub_i32 s91, s91, s90
	s_lshl_b32 s92, s90, 3
	s_sub_i32 s92, s61, s92
	s_mov_b32 s18, 0
	s_cmp_ge_u32 s92, s91
	s_cselect_b32 s93, s91, 0
	s_cselect_b32 s94, 1, 0
	s_sub_i32 s92, s92, s93
	s_add_i32 s18, s18, s94
	s_cmp_ge_u32 s92, s91
	s_cselect_b32 s93, s91, 0
	s_cselect_b32 s94, 1, 0
	s_sub_i32 s92, s92, s93
	s_add_i32 s18, s18, s94
	s_cmp_ge_u32 s92, s91
	s_cselect_b32 s93, s91, 0
	s_cselect_b32 s94, 1, 0
	s_sub_i32 s92, s92, s93
	s_add_i32 s18, s18, s94
	s_cmp_ge_u32 s92, s91
	s_cselect_b32 s93, s91, 0
	s_cselect_b32 s94, 1, 0
	s_sub_i32 s92, s92, s93
	s_add_i32 s18, s18, s94
	s_cmp_ge_u32 s92, s91
	s_cselect_b32 s93, s91, 0
	s_cselect_b32 s94, 1, 0
	s_sub_i32 s92, s92, s93
	s_add_i32 s18, s18, s94
	s_cmp_ge_u32 s92, s91
	s_cselect_b32 s93, s91, 0
	s_cselect_b32 s94, 1, 0
	s_sub_i32 s92, s92, s93
	s_add_i32 s18, s18, s94
	s_cmp_ge_u32 s92, s91
	s_cselect_b32 s93, s91, 0
	s_cselect_b32 s94, 1, 0
	s_sub_i32 s92, s92, s93
	s_add_i32 s18, s18, s94
	s_add_i32 s3, s90, s92
	s_and_b32 s99, s3, 1
	s_lshl_b32 s0, s3, 2
	s_add_i32 s0, s0, 0
	s_add_i32 s0, s0, 0x202e0
	v_mov_b32_e32 v4, s0
	ds_read_b32 v4, v4
	v_bitop3_b32 v1, v1, v2, 48 bitop3:0x6c
	v_lshrrev_b32_e32 v2, 3, v0
	s_lshl_b32 s20, s3, 8
	v_and_or_b32 v5, v2, 48, v3
	v_or_b32_e32 v2, 64, v2
	s_movk_i32 s0, 0x70
	s_ashr_i32 s21, s20, 31
	v_and_or_b32 v2, v2, s0, v3
	s_waitcnt lgkmcnt(0)
	v_lshlrev_b32_e32 v3, 2, v4
	s_lshl_b64 s[0:1], s[20:21], 11
	v_add_u32_e32 v3, 0, v3
	s_add_u32 s22, s62, s0
	v_add_u32_e32 v6, 0x20240, v3
	v_add_u32_e32 v3, 0x201c0, v3
	s_addc_u32 s23, s63, s1
	s_lshl_b32 s0, s9, 10
	v_and_or_b32 v1, v0, 64, v1
	ds_read_b32 v6, v6
	ds_read_b32 v3, v3
	s_add_i32 s21, s0, 0
	s_waitcnt vmcnt(0)
	s_add_i32 s67, s21, 0x2000
	v_lshl_or_b32 v180, v5, 11, v1
	s_waitcnt lgkmcnt(0)
	s_barrier
	s_mov_b32 m0, s21
	v_lshl_or_b32 v182, v2, 11, v1
	global_load_lds_dwordx4 v180, s[22:23]
	s_mov_b32 m0, s67
	s_waitcnt lgkmcnt(0)
	v_subrev_u32_e32 v1, s3, v6
	global_load_lds_dwordx4 v182, s[22:23]
	v_lshlrev_b32_e32 v1, 8, v1
	v_add_u32_e32 v1, v1, v3
	s_movk_i32 s3, 0x80
	s_movk_i32 s0, 0x81
	v_cmp_lt_i32_e32 vcc, s3, v1
	v_mov_b32_e32 v187, 0
	v_readfirstlane_b32 s2, v4
	v_cmp_gt_i32_e64 s[0:1], s0, v1
	v_or_b32_e32 v184, 0x40000, v180
	v_or_b32_e32 v186, 0x40000, v182
	v_mov_b32_e32 v185, v187
	s_cbranch_vccz .LBB0_852
	s_add_i32 m0, s21, 0x4000
	v_lshl_add_u64 v[2:3], s[22:23], 0, v[186:187]
	global_load_lds_dwordx4 v184, s[22:23]
	s_add_i32 m0, s21, 0x6000
	s_nop 0
	global_load_lds_dwordx4 v[2:3], off

.LBB0_853:
	s_add_i32 s0, s61, s33
	s_cmp_lt_i32 s61, s53
	s_cselect_b32 s1, s60, -1
	s_cmp_lt_i32 s0, s53
	s_cselect_b32 s61, s0, s1
	s_cmp_lt_i32 s61, 0
	s_cselect_b64 s[24:25], -1, 0
	s_and_b64 vcc, exec, s[24:25]
	s_mov_b32 s36, s18
	s_mov_b32 s42, s20
	s_cbranch_vccnz .LBB0_855
	s_lshr_b32 s89, s61, 3
	s_lshl_b32 s89, s89, 2
	s_add_i32 s89, s89, 0x202e0
	v_mov_b32_e32 v222, s89
	ds_read_b32 v222, v222
	s_waitcnt lgkmcnt(0)
	v_lshlrev_b32_e32 v222, 2, v222
	v_add_u32_e32 v222, 0x20240, v222
	ds_read2_b32 v[252:253], v222 offset1:1
	s_waitcnt lgkmcnt(0)
	v_readfirstlane_b32 s90, v252
	v_readfirstlane_b32 s91, v253
	s_nop 3
	s_sub_i32 s91, s91, s90
	s_lshl_b32 s92, s90, 3
	s_sub_i32 s92, s61, s92
	s_mov_b32 s36, 0
	s_cmp_ge_u32 s92, s91
	s_cselect_b32 s93, s91, 0
	s_cselect_b32 s94, 1, 0
	s_sub_i32 s92, s92, s93
	s_add_i32 s36, s36, s94
	s_cmp_ge_u32 s92, s91
	s_cselect_b32 s93, s91, 0
	s_cselect_b32 s94, 1, 0
	s_sub_i32 s92, s92, s93
	s_add_i32 s36, s36, s94
	s_cmp_ge_u32 s92, s91
	s_cselect_b32 s93, s91, 0
	s_cselect_b32 s94, 1, 0
	s_sub_i32 s92, s92, s93
	s_add_i32 s36, s36, s94
	s_cmp_ge_u32 s92, s91
	s_cselect_b32 s93, s91, 0
	s_cselect_b32 s94, 1, 0
	s_sub_i32 s92, s92, s93
	s_add_i32 s36, s36, s94
	s_cmp_ge_u32 s92, s91
	s_cselect_b32 s93, s91, 0
	s_cselect_b32 s94, 1, 0
	s_sub_i32 s92, s92, s93
	s_add_i32 s36, s36, s94
	s_cmp_ge_u32 s92, s91
	s_cselect_b32 s93, s91, 0
	s_cselect_b32 s94, 1, 0
	s_sub_i32 s92, s92, s93
	s_add_i32 s36, s36, s94
	s_cmp_ge_u32 s92, s91
	s_cselect_b32 s93, s91, 0
	s_cselect_b32 s94, 1, 0
	s_sub_i32 s92, s92, s93
	s_add_i32 s36, s36, s94
	s_add_i32 s2, s90, s92
	s_and_b32 s100, s2, 1
	s_lshl_b32 s0, s2, 2
	s_add_i32 s0, s0, 0
	s_add_i32 s0, s0, 0x202e0
	v_mov_b32_e32 v1, s0
	ds_read_b32 v1, v1
	s_ashr_i32 s37, s36, 31
	s_waitcnt lgkmcnt(0)
	v_lshlrev_b32_e32 v2, 2, v1
	v_add_u32_e32 v2, 0, v2
	v_readfirstlane_b32 s0, v1
	v_add_u32_e32 v3, 0x20240, v2
	s_ashr_i32 s1, s0, 31
	ds_read_b32 v3, v3
	s_lshl_b64 s[0:1], s[0:1], 23
	v_add_u32_e32 v2, 0x201c0, v2
	s_add_u32 s3, s54, s0
	ds_read_b32 v2, v2
	s_addc_u32 s27, s55, s1
	s_lshl_b32 s42, s2, 8
	s_lshl_b64 s[0:1], s[36:37], 10
	s_add_u32 s26, s3, s0
	s_addc_u32 s27, s27, s1
	s_waitcnt lgkmcnt(0)
	v_subrev_u32_e32 v1, s2, v3
	s_add_u32 s38, s26, 0x200
	v_lshlrev_b32_e32 v1, 8, v1
	s_addc_u32 s39, s27, 0
	s_ashr_i32 s43, s42, 31
	v_add_u32_e32 v1, v1, v2
	s_lshl_b64 s[0:1], s[42:43], 11
	v_cmp_gt_i32_e32 vcc, s19, v1
	s_add_u32 s40, s62, s0
	s_addc_u32 s41, s63, s1
	v_cndmask_b32_e64 v208, 0, 1, vcc

.LBB0_862:
	s_add_i32 s48, s48, 2
	s_cmp_eq_u32 s35, 12
	s_cselect_b32 s48, 0, s48
	s_cselect_b32 s77, s41, s23
	s_cselect_b32 s82, s40, s22
	s_cselect_b32 s35, s39, s47
	s_cselect_b32 s37, s38, s46
	s_cselect_b32 s43, s27, s45
	s_cselect_b32 s74, s26, s44
	s_cselect_b32 s101, s100, s99
	s_cselect_b64 vcc, -1, 0
	s_cmp_lg_u64 s[2:3], 0
	s_cbranch_scc1 .Lw2_dnE
	s_waitcnt vmcnt(4)
	s_branch .Lwd_dnE

.Lwd_dnE:
	v_cvt_pk_bf16_f32 v2, v64, v65
	v_cvt_pk_bf16_f32 v3, v66, v67
	s_ashr_i32 s49, s48, 31
	ds_write_b64 v199, v[2:3]
	v_cvt_pk_bf16_f32 v2, v60, v61
	v_cvt_pk_bf16_f32 v3, v62, v63
	s_lshl_b64 s[50:51], s[48:49], 19
	ds_write_b64 v200, v[2:3]
	v_cvt_pk_bf16_f32 v2, v76, v77
	v_cvt_pk_bf16_f32 v3, v78, v79
	s_add_u32 s72, s74, s50
	ds_write_b64 v201, v[2:3]
	v_cvt_pk_bf16_f32 v2, v72, v73
	v_cvt_pk_bf16_f32 v3, v74, v75
	s_addc_u32 s73, s43, s51
	ds_write_b64 v202, v[2:3]
	v_cvt_pk_bf16_f32 v2, v88, v89
	v_cvt_pk_bf16_f32 v3, v90, v91
	s_add_u32 s50, s37, s50
	ds_write_b64 v203, v[2:3]
	v_cvt_pk_bf16_f32 v2, v84, v85
	v_cvt_pk_bf16_f32 v3, v86, v87
	s_addc_u32 s51, s35, s51
	ds_write_b64 v204, v[2:3]
	v_cvt_pk_bf16_f32 v2, v96, v97
	v_cvt_pk_bf16_f32 v3, v98, v99
	s_add_u32 s78, s72, 0x4000
	ds_write_b64 v205, v[2:3]
	v_cvt_pk_bf16_f32 v2, v92, v93
	v_cvt_pk_bf16_f32 v3, v94, v95
	ds_write_b64 v206, v[2:3]
	s_addc_u32 s79, s73, 0
	s_cmp_lg_u32 s101, 0
	s_cbranch_scc1 .Lrot_dnE
	global_load_dwordx4 v[96:99], v189, s[72:73]
	global_load_dwordx4 v[88:91], v189, s[50:51]
	s_add_u32 s78, s72, 0x4000
	s_addc_u32 s79, s73, 0
	s_add_u32 s80, s50, 0x4000
	s_addc_u32 s81, s51, 0
	global_load_dwordx4 v[92:95], v189, s[78:79]
	global_load_dwordx4 v[76:79], v189, s[80:81]
	s_add_u32 s78, s72, 0x8000
	s_addc_u32 s79, s73, 0
	s_add_u32 s80, s50, 0x8000
	s_addc_u32 s81, s51, 0
	global_load_dwordx4 v[84:87], v189, s[78:79]
	global_load_dwordx4 v[64:67], v189, s[80:81]
	s_add_u32 s78, s72, 0xc000
	s_addc_u32 s79, s73, 0
	s_add_u32 s80, s50, 0xc000
	s_addc_u32 s81, s51, 0
	global_load_dwordx4 v[72:75], v189, s[78:79]
	global_load_dwordx4 v[60:63], v189, s[80:81]
	s_branch .Lrotd_dnE
.Lrot_dnE:
	s_add_u32 s78, s72, 0x8000
	s_addc_u32 s79, s73, 0
	s_add_u32 s80, s50, 0x8000
	s_addc_u32 s81, s51, 0
	global_load_dwordx4 v[84:87], v189, s[78:79]
	global_load_dwordx4 v[64:67], v189, s[80:81]
	s_add_u32 s78, s72, 0xc000
	s_addc_u32 s79, s73, 0
	s_add_u32 s80, s50, 0xc000
	s_addc_u32 s81, s51, 0
	global_load_dwordx4 v[72:75], v189, s[78:79]
	global_load_dwordx4 v[60:63], v189, s[80:81]
	global_load_dwordx4 v[96:99], v189, s[72:73]
	global_load_dwordx4 v[88:91], v189, s[50:51]
	s_add_u32 s78, s72, 0x4000
	s_addc_u32 s79, s73, 0
	s_add_u32 s80, s50, 0x4000
	s_addc_u32 s81, s51, 0
	global_load_dwordx4 v[92:95], v189, s[78:79]
	global_load_dwordx4 v[76:79], v189, s[80:81]
.Lrotd_dnE:
	s_lshl_b64 s[50:51], s[48:49], 7
	s_add_u32 s50, s82, s50
	s_addc_u32 s51, s77, s51
	s_mov_b32 m0, s21
	s_waitcnt vmcnt(8)
	s_waitcnt lgkmcnt(0)
	s_barrier
	v_lshl_add_u64 v[2:3], s[50:51], 0, v[180:181]
	global_load_lds_dwordx4 v[2:3], off
	v_lshl_add_u64 v[2:3], s[50:51], 0, v[182:183]
	s_mov_b32 m0, s67
	v_cndmask_b32_e32 v1, v209, v208, vcc
	global_load_lds_dwordx4 v[2:3], off
	v_cmp_ne_u32_e32 vcc, 0, v1
	s_mov_b64 s[96:97], vcc
	s_cbranch_vccnz .LBB0_864
	v_lshl_add_u64 v[164:165], s[50:51], 0, v[184:185]
	s_add_i32 m0, s21, 0x4000
	v_lshl_add_u64 v[2:3], s[50:51], 0, v[186:187]
	global_load_lds_dwordx4 v[164:165], off
	s_add_i32 m0, s21, 0x6000
	s_nop 0
	global_load_lds_dwordx4 v[2:3], off

.Lwd_dnO:
	s_add_u32 s48, s2, 0x80000
	v_cvt_pk_bf16_f32 v2, v96, v97
	v_cvt_pk_bf16_f32 v3, v98, v99
	ds_write_b64 v194, v[2:3]
	v_cvt_pk_bf16_f32 v2, v88, v89
	v_cvt_pk_bf16_f32 v3, v90, v91
	s_addc_u32 s49, s3, 0
	ds_write_b64 v194, v[2:3] offset:16384
	v_cvt_pk_bf16_f32 v2, v92, v93
	v_cvt_pk_bf16_f32 v3, v94, v95
	s_add_u32 s2, s74, s48
	ds_write_b64 v195, v[2:3]
	v_cvt_pk_bf16_f32 v2, v76, v77
	v_cvt_pk_bf16_f32 v3, v78, v79
	s_addc_u32 s3, s43, s49
	ds_write_b64 v195, v[2:3] offset:16384
	v_cvt_pk_bf16_f32 v2, v84, v85
	v_cvt_pk_bf16_f32 v3, v86, v87
	s_add_u32 s48, s37, s48
	ds_write_b64 v196, v[2:3]
	v_cvt_pk_bf16_f32 v2, v64, v65
	v_cvt_pk_bf16_f32 v3, v66, v67
	s_addc_u32 s49, s35, s49
	ds_write_b64 v196, v[2:3] offset:16384
	v_cvt_pk_bf16_f32 v2, v72, v73
	v_cvt_pk_bf16_f32 v3, v74, v75
	s_add_u32 s50, s2, 0x4000
	ds_write_b64 v197, v[2:3]
	v_cvt_pk_bf16_f32 v2, v60, v61
	v_cvt_pk_bf16_f32 v3, v62, v63
	ds_write_b64 v197, v[2:3] offset:16384
	s_addc_u32 s51, s3, 0
	s_cmp_lg_u32 s101, 0
	s_cbranch_scc1 .Lrot_dnO
	global_load_dwordx4 v[64:67], v189, s[2:3]
	global_load_dwordx4 v[60:63], v189, s[48:49]
	s_add_u32 s50, s2, 0x4000
	s_addc_u32 s51, s3, 0
	s_add_u32 s72, s48, 0x4000
	s_addc_u32 s73, s49, 0
	global_load_dwordx4 v[76:79], v189, s[50:51]
	global_load_dwordx4 v[72:75], v189, s[72:73]
	s_add_u32 s50, s2, 0x8000
	s_addc_u32 s51, s3, 0
	s_add_u32 s72, s48, 0x8000
	s_addc_u32 s73, s49, 0
	global_load_dwordx4 v[88:91], v189, s[50:51]
	global_load_dwordx4 v[84:87], v189, s[72:73]
	s_add_u32 s50, s2, 0xc000
	s_addc_u32 s51, s3, 0
	s_add_u32 s72, s48, 0xc000
	s_addc_u32 s73, s49, 0
	global_load_dwordx4 v[96:99], v189, s[50:51]
	global_load_dwordx4 v[92:95], v189, s[72:73]
	s_branch .Lrotd_dnO
.Lrot_dnO:
	s_add_u32 s50, s2, 0x8000
	s_addc_u32 s51, s3, 0
	s_add_u32 s72, s48, 0x8000
	s_addc_u32 s73, s49, 0
	global_load_dwordx4 v[88:91], v189, s[50:51]
	global_load_dwordx4 v[84:87], v189, s[72:73]
	s_add_u32 s50, s2, 0xc000
	s_addc_u32 s51, s3, 0
	s_add_u32 s72, s48, 0xc000
	s_addc_u32 s73, s49, 0
	global_load_dwordx4 v[96:99], v189, s[50:51]
	global_load_dwordx4 v[92:95], v189, s[72:73]
	global_load_dwordx4 v[64:67], v189, s[2:3]
	global_load_dwordx4 v[60:63], v189, s[48:49]
	s_add_u32 s50, s2, 0x4000
	s_addc_u32 s51, s3, 0
	s_add_u32 s72, s48, 0x4000
	s_addc_u32 s73, s49, 0
	global_load_dwordx4 v[76:79], v189, s[50:51]
	global_load_dwordx4 v[72:75], v189, s[72:73]
.Lrotd_dnO:
	s_waitcnt vmcnt(8)
	s_waitcnt lgkmcnt(0)
	s_barrier
	s_cmp_gt_u32 s34, 13
	s_cbranch_scc1 .LBB0_870
	s_mov_b32 s35, s34
	s_branch .LBB0_856
.LBB0_870:
	v_add_u32_e32 v164, s20, v188
	v_lshl_or_b32 v2, s18, 8, v198
	v_ashrrev_i32_e32 v165, 31, v164
	v_ashrrev_i32_e32 v3, 31, v2
	v_lshlrev_b64 v[166:167], 12, v[164:165]
	v_cvt_pk_bf16_f32 v160, v160, v161
	v_cvt_pk_bf16_f32 v161, v162, v163
	v_cvt_pk_bf16_f32 v162, v156, v157
	v_cvt_pk_bf16_f32 v163, v158, v159
	v_lshl_add_u64 v[156:157], s[6:7], 0, v[166:167]
	v_lshlrev_b64 v[158:159], 1, v[2:3]
	v_permlane16_swap_b32_e32 v160, v162
	v_permlane16_swap_b32_e32 v161, v163
	v_lshl_add_u64 v[2:3], v[156:157], 0, v[158:159]
	global_store_dwordx4 v[2:3], v[160:163], off
	v_cvt_pk_bf16_f32 v144, v144, v145
	v_cvt_pk_bf16_f32 v145, v146, v147
	v_cvt_pk_bf16_f32 v146, v140, v141
	v_cvt_pk_bf16_f32 v147, v142, v143
	v_or_b32_e32 v140, 16, v164
	v_permlane16_swap_b32_e32 v144, v146
	v_permlane16_swap_b32_e32 v145, v147
	v_ashrrev_i32_e32 v141, 31, v140
	global_store_dwordx4 v[2:3], v[144:147], off offset:256
	s_nop 1
	v_lshlrev_b64 v[144:145], 12, v[140:141]
	v_cvt_pk_bf16_f32 v140, v152, v153
	v_cvt_pk_bf16_f32 v141, v154, v155
	v_cvt_pk_bf16_f32 v142, v148, v149
	v_cvt_pk_bf16_f32 v143, v150, v151
	v_lshl_add_u64 v[144:145], s[6:7], 0, v[144:145]
	v_permlane16_swap_b32_e32 v140, v142
	v_permlane16_swap_b32_e32 v141, v143
	v_lshl_add_u64 v[144:145], v[144:145], 0, v[158:159]
	global_store_dwordx4 v[144:145], v[140:143], off
	v_cvt_pk_bf16_f32 v128, v128, v129
	v_cvt_pk_bf16_f32 v129, v130, v131
	v_cvt_pk_bf16_f32 v130, v124, v125
	v_cvt_pk_bf16_f32 v131, v126, v127
	v_or_b32_e32 v124, 32, v164
	v_permlane16_swap_b32_e32 v128, v130
	v_permlane16_swap_b32_e32 v129, v131
	v_ashrrev_i32_e32 v125, 31, v124
	global_store_dwordx4 v[144:145], v[128:131], off offset:256
	s_nop 1
	v_lshlrev_b64 v[128:129], 12, v[124:125]
	v_cvt_pk_bf16_f32 v124, v136, v137
	v_cvt_pk_bf16_f32 v125, v138, v139
	v_cvt_pk_bf16_f32 v126, v132, v133
	v_cvt_pk_bf16_f32 v127, v134, v135
	v_lshl_add_u64 v[128:129], s[6:7], 0, v[128:129]
	v_permlane16_swap_b32_e32 v124, v126
	v_permlane16_swap_b32_e32 v125, v127
	v_lshl_add_u64 v[128:129], v[128:129], 0, v[158:159]
	global_store_dwordx4 v[128:129], v[124:127], off
	v_cvt_pk_bf16_f32 v112, v112, v113
	v_cvt_pk_bf16_f32 v113, v114, v115
	v_cvt_pk_bf16_f32 v114, v108, v109
	v_cvt_pk_bf16_f32 v115, v110, v111
	v_or_b32_e32 v108, 48, v164
	v_permlane16_swap_b32_e32 v112, v114
	v_permlane16_swap_b32_e32 v113, v115
	v_ashrrev_i32_e32 v109, 31, v108
	global_store_dwordx4 v[128:129], v[112:115], off offset:256
	s_nop 1
	v_lshlrev_b64 v[112:113], 12, v[108:109]
	v_cvt_pk_bf16_f32 v108, v120, v121
	v_cvt_pk_bf16_f32 v109, v122, v123
	v_cvt_pk_bf16_f32 v110, v116, v117
	v_cvt_pk_bf16_f32 v111, v118, v119
	v_lshl_add_u64 v[112:113], s[6:7], 0, v[112:113]
	v_permlane16_swap_b32_e32 v108, v110
	v_permlane16_swap_b32_e32 v109, v111
	v_lshl_add_u64 v[112:113], v[112:113], 0, v[158:159]
	global_store_dwordx4 v[112:113], v[108:111], off
	v_cvt_pk_bf16_f32 v104, v104, v105
	v_cvt_pk_bf16_f32 v105, v106, v107
	v_cvt_pk_bf16_f32 v106, v100, v101
	v_cvt_pk_bf16_f32 v107, v102, v103
	s_nop 0
	v_permlane16_swap_b32_e32 v104, v106
	v_permlane16_swap_b32_e32 v105, v107
	global_store_dwordx4 v[112:113], v[104:107], off offset:256
	v_cvt_pk_bf16_f32 v80, v80, v81
	v_cvt_pk_bf16_f32 v81, v82, v83
	v_cvt_pk_bf16_f32 v82, v68, v69
	v_cvt_pk_bf16_f32 v83, v70, v71
	v_add_co_u32_e32 v70, vcc, s68, v2
	v_permlane16_swap_b32_e32 v80, v82
	v_permlane16_swap_b32_e32 v81, v83
	v_addc_co_u32_e32 v71, vcc, 0, v3, vcc
	global_store_dwordx4 v[70:71], v[80:83], off
	v_cvt_pk_bf16_f32 v56, v56, v57
	v_cvt_pk_bf16_f32 v57, v58, v59
	v_cvt_pk_bf16_f32 v58, v52, v53
	v_cvt_pk_bf16_f32 v59, v54, v55
	v_lshl_add_u64 v[68:69], v[2:3], 0, s[8:9]
	v_permlane16_swap_b32_e32 v56, v58
	v_permlane16_swap_b32_e32 v57, v59
	global_store_dwordx4 v[68:69], v[56:59], off offset:256
	v_cvt_pk_bf16_f32 v48, v48, v49
	v_cvt_pk_bf16_f32 v49, v50, v51
	v_cvt_pk_bf16_f32 v50, v44, v45
	v_cvt_pk_bf16_f32 v51, v46, v47
	v_add_co_u32_e32 v46, vcc, s69, v2
	v_permlane16_swap_b32_e32 v48, v50
	v_permlane16_swap_b32_e32 v49, v51
	v_addc_co_u32_e32 v47, vcc, 0, v3, vcc
	global_store_dwordx4 v[46:47], v[48:51], off
	v_cvt_pk_bf16_f32 v40, v40, v41
	v_cvt_pk_bf16_f32 v41, v42, v43
	v_cvt_pk_bf16_f32 v42, v36, v37
	v_cvt_pk_bf16_f32 v43, v38, v39
	v_lshl_add_u64 v[44:45], v[2:3], 0, s[12:13]
	v_permlane16_swap_b32_e32 v40, v42
	v_permlane16_swap_b32_e32 v41, v43
	global_store_dwordx4 v[44:45], v[40:43], off offset:256
	v_cvt_pk_bf16_f32 v32, v32, v33
	v_cvt_pk_bf16_f32 v33, v34, v35
	v_cvt_pk_bf16_f32 v34, v28, v29
	v_cvt_pk_bf16_f32 v35, v30, v31
	v_add_co_u32_e32 v30, vcc, s70, v2
	v_permlane16_swap_b32_e32 v32, v34
	v_permlane16_swap_b32_e32 v33, v35
	v_addc_co_u32_e32 v31, vcc, 0, v3, vcc
	global_store_dwordx4 v[30:31], v[32:35], off
	v_cvt_pk_bf16_f32 v24, v24, v25
	v_cvt_pk_bf16_f32 v25, v26, v27
	v_cvt_pk_bf16_f32 v26, v20, v21
	v_cvt_pk_bf16_f32 v27, v22, v23
	v_lshl_add_u64 v[28:29], v[2:3], 0, s[14:15]
	v_permlane16_swap_b32_e32 v24, v26
	v_permlane16_swap_b32_e32 v25, v27
	global_store_dwordx4 v[28:29], v[24:27], off offset:256
	v_cvt_pk_bf16_f32 v16, v16, v17
	v_cvt_pk_bf16_f32 v17, v18, v19
	v_cvt_pk_bf16_f32 v18, v12, v13
	v_cvt_pk_bf16_f32 v19, v14, v15
	v_lshl_add_u64 v[12:13], v[2:3], 0, s[16:17]
	v_add_co_u32_e32 v2, vcc, s71, v2
	v_permlane16_swap_b32_e32 v16, v18
	v_permlane16_swap_b32_e32 v17, v19
	v_addc_co_u32_e32 v3, vcc, 0, v3, vcc
	global_store_dwordx4 v[2:3], v[16:19], off
	v_cvt_pk_bf16_f32 v2, v8, v9
	v_cvt_pk_bf16_f32 v3, v10, v11
	v_cvt_pk_bf16_f32 v4, v4, v5
	v_cvt_pk_bf16_f32 v5, v6, v7
	s_and_b64 vcc, exec, s[24:25]
	v_permlane16_swap_b32_e32 v2, v4
	v_permlane16_swap_b32_e32 v3, v5
	global_store_dwordx4 v[12:13], v[2:5], off offset:256
	s_cbranch_vccnz .LBB0_872
	v_mov_b32_e32 v209, v208
	s_mov_b32 s20, s42
	s_mov_b32 s18, s36
	s_mov_b64 s[22:23], s[40:41]
	s_mov_b64 s[46:47], s[38:39]
	s_mov_b64 s[44:45], s[26:27]
	s_mov_b32 s99, s100
	s_branch .LBB0_853
